# adds in-proj epilogue: row-stat loads issued 4 rows ahead with counted vmcnt
# baseline (speedup 1.0000x reference)
; __device__ __forceinline__ float sigm(float x) { return __builtin_amdgcn_rcpf(1.f + __builtin_amdgcn_exp2f(-1.4426950408889634f * x)); }
; __device__ __forceinline__ float gelu_t(float x) { const float u = 0.7978845608028654f * (x + 0.044715f * x * x * x); return x * sigm(2.f * u); }
; __device__ __forceinline__ u32x4 pack8(f32x4 v0, f32x4 v1) { u32x4 w; w.x = cvt_pk_bf16(v0[0], v0[1]); w.y = cvt_pk_bf16(v0[2], v0[3]); w.z = cvt_pk_bf16(v1[0], v1[1]); w.w = cvt_pk_bf16(v1[2], v1[3]); return w; }
; template <class T> __device__ __forceinline__ void est(T* p, T v) { if constexpr (MK_EPI_NT != 0) __builtin_nontemporal_store(v, p); else *p = v; }
; __device__ __forceinline__ unsigned pk4_u8(f32x4 v) { return q8(v[0]) | (q8(v[1]) << 8) | (q8(v[2]) << 16) | (q8(v[3]) << 24); }
; __device__ __forceinline__ float ss_val(const ss_t* ss, int row) { return (float)ss[row] * (1.f / 16777216.f); }
;     __device__ __forceinline__ void operator()(AccT acc, const Unit& u, int wr, int wc, int fr, int fq) const {
;         const int type = u.pn < 10 ? 0 : (u.pn < 14 ? 1 : (u.pn < 18 ? 2 : 3));
;         const int row0 = u.pm * 256 + wr * 64 + fr, col0 = u.pn * 256 + wc * 32 + 8 * fq;
; #pragma unroll
;         for (int ai = 0; ai < 2; ++ai)
; #pragma unroll
;             for (int m = 0; m < 4; ++m) { const int row = row0 + ai * 128 + m * 16; const float r = rsqrtf(ss_val(ss, row) * (1.0f / DM) + EPS); bf16_t* rp = O + (size_t)row * NIN + col0; float sq = 0.f;
; #pragma unroll
;                 for (int bj = 0; bj < 2; ++bj) { f32x4 v0 = acc[ai][bj][m][0] * r, v1 = acc[ai][bj][m][1] * r;
;                     if (type == 1 || type == 2) {
; #pragma unroll
;                         for (int j = 0; j < 4; ++j) { v0[j] = gelu_t(v0[j]); v1[j] = gelu_t(v1[j]); }
;                         if (type == 2) sq += sum8sq(v0, v1); }
;                     if (type == 3) {
; #pragma unroll
;                         for (int j = 0; j < 4; ++j) { v0[j] = sigm(v0[j]); v1[j] = sigm(v1[j]); }
;                         est((u32x2*)(G8 + (size_t)row * (NIN - C_G) + (col0 - C_G) + bj * 128), (u32x2)(u32x2){pk4_u8(v0), pk4_u8(v1)}); }
;                     else est((u32x4*)(rp + bj * 128), (u32x4)pack8(v0, v1)); }
;                 if (type == 2) row_atomic(ssv, row, sq, fq); }
;     }
.LBB0_383:
	v_lshl_add_u32 v146, s8, 8, v158
	v_ashrrev_i32_e32 v147, 31, v146
	v_lshl_add_u64 v[148:149], v[146:147], 3, s[26:27]
	global_load_dwordx2 v[248:249], v[148:149], off
	global_load_dwordx2 v[250:251], v[148:149], off offset:128
	global_load_dwordx2 v[252:253], v[148:149], off offset:256
	global_load_dwordx2 v[254:255], v[148:149], off offset:384
	s_cmp_lt_u32 s16, 18
	s_cselect_b32 s8, 2, 3
	s_cmp_gt_u32 s16, 13
	s_cselect_b32 s8, s8, 1
	s_cmp_gt_i32 s16, 9
	s_cselect_b32 s12, s8, 0
	s_cmp_eq_u32 s12, 2
	s_cselect_b64 s[10:11], -1, 0
	s_add_i32 s13, s12, -1
	s_cmp_lt_u32 s13, 2
	s_cselect_b64 s[8:9], -1, 0
	s_cmp_gt_u32 s13, 1
	v_mov_b32_e32 v167, 0
	s_waitcnt vmcnt(3)
	v_mov_b32_e32 v150, v248
	v_mov_b32_e32 v151, v249
	global_load_dwordx2 v[248:249], v[148:149], off offset:1024
	v_ffbh_u32_e32 v152, v151
	v_min_u32_e32 v152, 32, v152
	v_lshlrev_b64 v[150:151], v152, v[150:151]
	v_min_u32_e32 v150, 1, v150
	v_or_b32_e32 v150, v151, v150
	v_cvt_f32_u32_e32 v150, v150
	v_sub_u32_e32 v151, 32, v152
	v_ldexp_f32 v150, v150, v151
	v_mul_f32_e32 v150, 0x33800000, v150
	v_fmamk_f32 v150, v150, 0x3a000000, v164
	v_mul_f32_e32 v151, 0x4b800000, v150
	v_cmp_gt_f32_e32 vcc, s89, v150
	s_nop 1
	v_cndmask_b32_e32 v150, v150, v151, vcc
	v_rsq_f32_e32 v150, v150
	s_nop 0
	v_mul_f32_e32 v151, 0x45800000, v150
	v_cndmask_b32_e32 v150, v150, v151, vcc
	v_pk_mul_f32 v[128:129], v[128:129], v[150:151] op_sel_hi:[1,0]
	v_pk_mul_f32 v[156:157], v[126:127], v[150:151] op_sel_hi:[1,0]
	v_pk_mul_f32 v[152:153], v[124:125], v[150:151] op_sel_hi:[1,0]
	v_pk_mul_f32 v[154:155], v[122:123], v[150:151] op_sel_hi:[1,0]
	s_cbranch_scc1 .LBB0_385
	v_mul_f32_e32 v123, 0x3d372713, v154
	v_mul_f32_e32 v123, v154, v123
	v_mul_f32_e32 v124, 0x3d372713, v157
	v_fma_f32 v123, v154, v123, v154
	v_mul_f32_e32 v124, v157, v124
	v_mul_f32_e32 v125, 0x3d372713, v155
	v_mul_f32_e32 v123, 0x3f4c422a, v123
	v_fma_f32 v124, v157, v124, v157
	v_mul_f32_e32 v125, v155, v125
	v_add_f32_e32 v123, v123, v123
	v_mul_f32_e32 v124, 0x3f4c422a, v124
	v_fma_f32 v125, v155, v125, v155
	v_mul_f32_e32 v123, 0xbfb8aa3b, v123
	v_add_f32_e32 v124, v124, v124
	v_mul_f32_e32 v125, 0x3f4c422a, v125
	v_exp_f32_e32 v123, v123
	v_mul_f32_e32 v124, 0xbfb8aa3b, v124
	v_add_f32_e32 v125, v125, v125
	v_exp_f32_e32 v124, v124
	v_mul_f32_e32 v125, 0xbfb8aa3b, v125
	v_exp_f32_e32 v127, v125
	v_add_f32_e32 v123, 1.0, v123
	v_rcp_f32_e32 v125, v123
	v_add_f32_e32 v123, 1.0, v124
	v_rcp_f32_e32 v126, v123
	v_add_f32_e32 v123, 1.0, v127
	v_mul_f32_e32 v124, 0x3d372713, v128
	v_mul_f32_e32 v127, 0x3d372713, v152
	v_mul_f32_e32 v124, v128, v124
	v_mul_f32_e32 v127, v152, v127
	v_fma_f32 v124, v128, v124, v128
	v_fma_f32 v127, v152, v127, v152
	v_mul_f32_e32 v124, 0x3f4c422a, v124
	v_mul_f32_e32 v127, 0x3f4c422a, v127
	v_add_f32_e32 v124, v124, v124
	v_add_f32_e32 v127, v127, v127
	v_mul_f32_e32 v124, 0xbfb8aa3b, v124
	v_mul_f32_e32 v127, 0xbfb8aa3b, v127
	v_exp_f32_e32 v124, v124
	v_exp_f32_e32 v127, v127
	v_rcp_f32_e32 v169, v123
	v_mul_f32_e32 v122, 0x3d372713, v156
	v_add_f32_e32 v123, 1.0, v124
	v_add_f32_e32 v124, 1.0, v127
	v_mul_f32_e32 v127, 0x3d372713, v129
	v_mul_f32_e32 v127, v129, v127
	v_mul_f32_e32 v151, 0x3d372713, v153
	v_mul_f32_e32 v122, v156, v122
	v_fma_f32 v127, v129, v127, v129
	v_mul_f32_e32 v151, v153, v151
	v_fma_f32 v122, v156, v122, v156
	v_mul_f32_e32 v127, 0x3f4c422a, v127
	v_fma_f32 v151, v153, v151, v153
	v_mul_f32_e32 v122, 0x3f4c422a, v122
	v_add_f32_e32 v127, v127, v127
	v_mul_f32_e32 v151, 0x3f4c422a, v151
	v_add_f32_e32 v122, v122, v122
	v_mul_f32_e32 v127, 0xbfb8aa3b, v127
	v_add_f32_e32 v151, v151, v151
	v_mul_f32_e32 v122, 0xbfb8aa3b, v122
	v_exp_f32_e32 v127, v127
	v_mul_f32_e32 v151, 0xbfb8aa3b, v151
	v_exp_f32_e32 v122, v122
	v_exp_f32_e32 v151, v151
	v_add_f32_e32 v127, 1.0, v127
	v_rcp_f32_e32 v127, v127
	v_add_f32_e32 v122, 1.0, v122
	v_add_f32_e32 v151, 1.0, v151
	v_rcp_f32_e32 v122, v122
	v_rcp_f32_e32 v123, v123
	v_rcp_f32_e32 v168, v151
	v_rcp_f32_e32 v124, v124
	v_mov_b32_e32 v171, v128
	v_mov_b32_e32 v128, v157
	v_mov_b32_e32 v170, v156
	v_pk_mul_f32 v[128:129], v[128:129], v[126:127]
	v_mov_b32_e32 v157, v154
	v_mov_b32_e32 v154, v153
	v_pk_mul_f32 v[122:123], v[170:171], v[122:123]
	v_pk_mul_f32 v[126:127], v[128:129], v[128:129]
	v_mov_b32_e32 v156, v152
	v_pk_mul_f32 v[168:169], v[154:155], v[168:169]
	v_pk_fma_f32 v[126:127], v[122:123], v[122:123], v[126:127]
	v_pk_mul_f32 v[124:125], v[156:157], v[124:125]
	v_pk_mul_f32 v[152:153], v[168:169], v[168:169]
	v_add_f32_e32 v126, v126, v127
	v_pk_fma_f32 v[152:153], v[124:125], v[124:125], v[152:153]
	v_mov_b32_e32 v156, v122
	v_add_f32_e32 v126, v153, v126
	v_add_f32_e32 v126, v152, v126
	v_cndmask_b32_e64 v167, 0, v126, s[10:11]
	v_mov_b32_e32 v157, v128
	v_mov_b32_e32 v128, v123
	v_mov_b32_e32 v154, v125
	v_mov_b32_e32 v155, v169
	v_mov_b32_e32 v152, v124
	v_mov_b32_e32 v153, v168

; __device__ __forceinline__ float sigm(float x) { return __builtin_amdgcn_rcpf(1.f + __builtin_amdgcn_exp2f(-1.4426950408889634f * x)); }
; __device__ __forceinline__ float gelu_t(float x) { const float u = 0.7978845608028654f * (x + 0.044715f * x * x * x); return x * sigm(2.f * u); }
; __device__ __forceinline__ u32x4 pack8(f32x4 v0, f32x4 v1) { u32x4 w; w.x = cvt_pk_bf16(v0[0], v0[1]); w.y = cvt_pk_bf16(v0[2], v0[3]); w.z = cvt_pk_bf16(v1[0], v1[1]); w.w = cvt_pk_bf16(v1[2], v1[3]); return w; }
; template <class T> __device__ __forceinline__ void est(T* p, T v) { if constexpr (MK_EPI_NT != 0) __builtin_nontemporal_store(v, p); else *p = v; }
; __device__ __forceinline__ unsigned pk4_u8(f32x4 v) { return q8(v[0]) | (q8(v[1]) << 8) | (q8(v[2]) << 16) | (q8(v[3]) << 24); }
; __device__ __forceinline__ float sum8sq(f32x4 a, f32x4 b) { return (a[0] * a[0] + a[1] * a[1]) + (a[2] * a[2] + a[3] * a[3]) + (b[0] * b[0] + b[1] * b[1]) + (b[2] * b[2] + b[3] * b[3]); }
; __device__ __forceinline__ float ss_val(const ss_t* ss, int row) { return (float)ss[row] * (1.f / 16777216.f); }
;     __device__ __forceinline__ void operator()(AccT acc, const Unit& u, int wr, int wc, int fr, int fq) const {
;     ...
;             for (int m = 0; m < 4; ++m) { const int row = row0 + ai * 128 + m * 16; const float r = rsqrtf(ss_val(ss, row) * (1.0f / DM) + EPS); bf16_t* rp = O + (size_t)row * NIN + col0; float sq = 0.f;
; #pragma unroll
;                 for (int bj = 0; bj < 2; ++bj) { f32x4 v0 = acc[ai][bj][m][0] * r, v1 = acc[ai][bj][m][1] * r;
;                     if (type == 1 || type == 2) {
; #pragma unroll
;                         for (int j = 0; j < 4; ++j) { v0[j] = gelu_t(v0[j]); v1[j] = gelu_t(v1[j]); }
;                         if (type == 2) sq += sum8sq(v0, v1); }
;                     if (type == 3) {
; #pragma unroll
;                         for (int j = 0; j < 4; ++j) { v0[j] = sigm(v0[j]); v1[j] = sigm(v1[j]); }
;                         est((u32x2*)(G8 + (size_t)row * (NIN - C_G) + (col0 - C_G) + bj * 128), (u32x2)(u32x2){pk4_u8(v0), pk4_u8(v1)}); }
;                     else est((u32x4*)(rp + bj * 128), (u32x4)pack8(v0, v1)); }
;                 if (type == 2) row_atomic(ssv, row, sq, fq); }
.LBB0_401:
	v_or_b32_e32 v114, 16, v146
	s_waitcnt lgkmcnt(0)
	v_ashrrev_i32_e32 v115, 31, v114
	v_lshl_add_u64 v[116:117], v[114:115], 3, s[26:27]
	s_nop 0
	s_and_b64 vcc, exec, s[12:13]
	v_mov_b32_e32 v124, 0
	s_waitcnt vmcnt(3)
	v_mov_b32_e32 v116, v250
	v_mov_b32_e32 v117, v251
	global_load_dwordx2 v[250:251], v[148:149], off offset:1152
	v_ffbh_u32_e32 v118, v117
	v_min_u32_e32 v118, 32, v118
	v_lshlrev_b64 v[116:117], v118, v[116:117]
	v_min_u32_e32 v116, 1, v116
	v_or_b32_e32 v116, v117, v116
	v_cvt_f32_u32_e32 v116, v116
	v_sub_u32_e32 v117, 32, v118
	v_ldexp_f32 v116, v116, v117
	v_mul_f32_e32 v116, 0x33800000, v116
	v_fmamk_f32 v116, v116, 0x3a000000, v164
	v_mul_f32_e32 v117, 0x4b800000, v116
	v_cmp_gt_f32_e64 s[16:17], s89, v116
	s_nop 1
	v_cndmask_b32_e64 v116, v116, v117, s[16:17]
	v_rsq_f32_e32 v116, v116
	s_nop 0
	v_mul_f32_e32 v117, 0x45800000, v116
	v_cndmask_b32_e64 v116, v116, v117, s[16:17]
	v_pk_mul_f32 v[112:113], v[112:113], v[116:117] op_sel_hi:[1,0]
	v_pk_mul_f32 v[120:121], v[110:111], v[116:117] op_sel_hi:[1,0]
	v_pk_mul_f32 v[110:111], v[108:109], v[116:117] op_sel_hi:[1,0]
	v_pk_mul_f32 v[118:119], v[106:107], v[116:117] op_sel_hi:[1,0]
	s_cbranch_vccnz .LBB0_403
	v_mul_f32_e32 v107, 0x3d372713, v118
	v_mul_f32_e32 v107, v118, v107
	v_mul_f32_e32 v108, 0x3d372713, v121
	v_fma_f32 v107, v118, v107, v118
	v_mul_f32_e32 v108, v121, v108
	v_mul_f32_e32 v109, 0x3d372713, v119
	v_mul_f32_e32 v107, 0x3f4c422a, v107
	v_fma_f32 v108, v121, v108, v121
	v_mul_f32_e32 v109, v119, v109
	v_add_f32_e32 v107, v107, v107
	v_mul_f32_e32 v108, 0x3f4c422a, v108
	v_fma_f32 v109, v119, v109, v119
	v_mul_f32_e32 v107, 0xbfb8aa3b, v107
	v_add_f32_e32 v108, v108, v108
	v_mul_f32_e32 v109, 0x3f4c422a, v109
	v_exp_f32_e32 v107, v107
	v_mul_f32_e32 v108, 0xbfb8aa3b, v108
	v_add_f32_e32 v109, v109, v109
	v_exp_f32_e32 v108, v108
	v_mul_f32_e32 v109, 0xbfb8aa3b, v109
	v_exp_f32_e32 v117, v109
	v_add_f32_e32 v107, 1.0, v107
	v_rcp_f32_e32 v109, v107
	v_add_f32_e32 v107, 1.0, v108
	v_rcp_f32_e32 v124, v107
	v_add_f32_e32 v107, 1.0, v117
	v_mul_f32_e32 v108, 0x3d372713, v112
	v_mul_f32_e32 v117, 0x3d372713, v110
	v_mul_f32_e32 v108, v112, v108
	v_mul_f32_e32 v117, v110, v117
	v_fma_f32 v108, v112, v108, v112
	v_fma_f32 v117, v110, v117, v110
	v_mul_f32_e32 v108, 0x3f4c422a, v108
	v_mul_f32_e32 v117, 0x3f4c422a, v117
	v_add_f32_e32 v108, v108, v108
	v_add_f32_e32 v117, v117, v117
	v_mul_f32_e32 v108, 0xbfb8aa3b, v108
	v_mul_f32_e32 v117, 0xbfb8aa3b, v117
	v_exp_f32_e32 v108, v108
	v_exp_f32_e32 v117, v117
	v_rcp_f32_e32 v127, v107
	v_mul_f32_e32 v106, 0x3d372713, v120
	v_add_f32_e32 v107, 1.0, v108
	v_add_f32_e32 v108, 1.0, v117
	v_mul_f32_e32 v117, 0x3d372713, v113
	v_mul_f32_e32 v117, v113, v117
	v_mul_f32_e32 v125, 0x3d372713, v111
	v_mul_f32_e32 v106, v120, v106
	v_fma_f32 v117, v113, v117, v113
	v_mul_f32_e32 v125, v111, v125
	v_fma_f32 v106, v120, v106, v120
	v_mul_f32_e32 v117, 0x3f4c422a, v117
	v_fma_f32 v125, v111, v125, v111
	v_mul_f32_e32 v106, 0x3f4c422a, v106
	v_add_f32_e32 v117, v117, v117
	v_mul_f32_e32 v125, 0x3f4c422a, v125
	v_add_f32_e32 v106, v106, v106
	v_mul_f32_e32 v117, 0xbfb8aa3b, v117
	v_add_f32_e32 v125, v125, v125
	v_mul_f32_e32 v106, 0xbfb8aa3b, v106
	v_exp_f32_e32 v117, v117
	v_mul_f32_e32 v125, 0xbfb8aa3b, v125
	v_exp_f32_e32 v106, v106
	v_exp_f32_e32 v126, v125
	v_add_f32_e32 v117, 1.0, v117
	v_rcp_f32_e32 v125, v117
	v_add_f32_e32 v106, 1.0, v106
	v_add_f32_e32 v117, 1.0, v126
	v_rcp_f32_e32 v106, v106
	v_rcp_f32_e32 v107, v107
	v_rcp_f32_e32 v126, v117
	v_rcp_f32_e32 v108, v108
	v_mov_b32_e32 v129, v112
	v_mov_b32_e32 v112, v121
	v_mov_b32_e32 v128, v120
	v_pk_mul_f32 v[112:113], v[112:113], v[124:125]
	v_mov_b32_e32 v125, v118
	v_mov_b32_e32 v118, v111
	v_pk_mul_f32 v[106:107], v[128:129], v[106:107]
	v_pk_mul_f32 v[120:121], v[112:113], v[112:113]
	v_mov_b32_e32 v124, v110
	v_pk_mul_f32 v[126:127], v[118:119], v[126:127]
	v_pk_fma_f32 v[120:121], v[106:107], v[106:107], v[120:121]
	v_pk_mul_f32 v[108:109], v[124:125], v[108:109]
	v_pk_mul_f32 v[110:111], v[126:127], v[126:127]
	v_add_f32_e32 v117, v120, v121
	v_pk_fma_f32 v[110:111], v[108:109], v[108:109], v[110:111]
	v_mov_b32_e32 v120, v106
	v_add_f32_e32 v111, v111, v117
	v_add_f32_e32 v110, v110, v111
	v_cndmask_b32_e64 v124, 0, v110, s[10:11]
	v_mov_b32_e32 v121, v112
	v_mov_b32_e32 v112, v107
	v_mov_b32_e32 v118, v109
	v_mov_b32_e32 v119, v127
	v_mov_b32_e32 v110, v108
	v_mov_b32_e32 v111, v126

; __device__ __forceinline__ float sigm(float x) { return __builtin_amdgcn_rcpf(1.f + __builtin_amdgcn_exp2f(-1.4426950408889634f * x)); }
; __device__ __forceinline__ float gelu_t(float x) { const float u = 0.7978845608028654f * (x + 0.044715f * x * x * x); return x * sigm(2.f * u); }
; __device__ __forceinline__ u32x4 pack8(f32x4 v0, f32x4 v1) { u32x4 w; w.x = cvt_pk_bf16(v0[0], v0[1]); w.y = cvt_pk_bf16(v0[2], v0[3]); w.z = cvt_pk_bf16(v1[0], v1[1]); w.w = cvt_pk_bf16(v1[2], v1[3]); return w; }
; template <class T> __device__ __forceinline__ void est(T* p, T v) { if constexpr (MK_EPI_NT != 0) __builtin_nontemporal_store(v, p); else *p = v; }
; __device__ __forceinline__ unsigned pk4_u8(f32x4 v) { return q8(v[0]) | (q8(v[1]) << 8) | (q8(v[2]) << 16) | (q8(v[3]) << 24); }
; __device__ __forceinline__ float sum8sq(f32x4 a, f32x4 b) { return (a[0] * a[0] + a[1] * a[1]) + (a[2] * a[2] + a[3] * a[3]) + (b[0] * b[0] + b[1] * b[1]) + (b[2] * b[2] + b[3] * b[3]); }
; __device__ __forceinline__ float ss_val(const ss_t* ss, int row) { return (float)ss[row] * (1.f / 16777216.f); }
;     __device__ __forceinline__ void operator()(AccT acc, const Unit& u, int wr, int wc, int fr, int fq) const {
;     ...
;             for (int m = 0; m < 4; ++m) { const int row = row0 + ai * 128 + m * 16; const float r = rsqrtf(ss_val(ss, row) * (1.0f / DM) + EPS); bf16_t* rp = O + (size_t)row * NIN + col0; float sq = 0.f;
; #pragma unroll
;                 for (int bj = 0; bj < 2; ++bj) { f32x4 v0 = acc[ai][bj][m][0] * r, v1 = acc[ai][bj][m][1] * r;
;                     if (type == 1 || type == 2) {
; #pragma unroll
;                         for (int j = 0; j < 4; ++j) { v0[j] = gelu_t(v0[j]); v1[j] = gelu_t(v1[j]); }
;                         if (type == 2) sq += sum8sq(v0, v1); }
;                     if (type == 3) {
; #pragma unroll
;                         for (int j = 0; j < 4; ++j) { v0[j] = sigm(v0[j]); v1[j] = sigm(v1[j]); }
;                         est((u32x2*)(G8 + (size_t)row * (NIN - C_G) + (col0 - C_G) + bj * 128), (u32x2)(u32x2){pk4_u8(v0), pk4_u8(v1)}); }
;                     else est((u32x4*)(rp + bj * 128), (u32x4)pack8(v0, v1)); }
;                 if (type == 2) row_atomic(ssv, row, sq, fq); }
.LBB0_419:
	v_or_b32_e32 v98, 32, v146
	s_waitcnt lgkmcnt(0)
	v_ashrrev_i32_e32 v99, 31, v98
	v_lshl_add_u64 v[100:101], v[98:99], 3, s[26:27]
	s_nop 0
	s_and_b64 vcc, exec, s[12:13]
	v_mov_b32_e32 v106, 0
	s_waitcnt vmcnt(3)
	v_mov_b32_e32 v100, v252
	v_mov_b32_e32 v101, v253
	global_load_dwordx2 v[252:253], v[148:149], off offset:1280
	v_ffbh_u32_e32 v102, v101
	v_min_u32_e32 v102, 32, v102
	v_lshlrev_b64 v[100:101], v102, v[100:101]
	v_min_u32_e32 v100, 1, v100
	v_or_b32_e32 v100, v101, v100
	v_cvt_f32_u32_e32 v100, v100
	v_sub_u32_e32 v101, 32, v102
	v_ldexp_f32 v100, v100, v101
	v_mul_f32_e32 v100, 0x33800000, v100
	v_fmamk_f32 v100, v100, 0x3a000000, v164
	v_mul_f32_e32 v101, 0x4b800000, v100
	v_cmp_gt_f32_e64 s[16:17], s89, v100
	s_nop 1
	v_cndmask_b32_e64 v100, v100, v101, s[16:17]
	v_rsq_f32_e32 v100, v100
	s_nop 0
	v_mul_f32_e32 v101, 0x45800000, v100
	v_cndmask_b32_e64 v100, v100, v101, s[16:17]
	v_pk_mul_f32 v[96:97], v[96:97], v[100:101] op_sel_hi:[1,0]
	v_pk_mul_f32 v[104:105], v[94:95], v[100:101] op_sel_hi:[1,0]
	v_pk_mul_f32 v[94:95], v[92:93], v[100:101] op_sel_hi:[1,0]
	v_pk_mul_f32 v[102:103], v[90:91], v[100:101] op_sel_hi:[1,0]
	s_cbranch_vccnz .LBB0_421
	v_mul_f32_e32 v91, 0x3d372713, v102
	v_mul_f32_e32 v91, v102, v91
	v_mul_f32_e32 v92, 0x3d372713, v105
	v_fma_f32 v91, v102, v91, v102
	v_mul_f32_e32 v92, v105, v92
	v_mul_f32_e32 v93, 0x3d372713, v103
	v_mul_f32_e32 v91, 0x3f4c422a, v91
	v_fma_f32 v92, v105, v92, v105
	v_mul_f32_e32 v93, v103, v93
	v_add_f32_e32 v91, v91, v91
	v_mul_f32_e32 v92, 0x3f4c422a, v92
	v_fma_f32 v93, v103, v93, v103
	v_mul_f32_e32 v91, 0xbfb8aa3b, v91
	v_add_f32_e32 v92, v92, v92
	v_mul_f32_e32 v93, 0x3f4c422a, v93
	v_exp_f32_e32 v91, v91
	v_mul_f32_e32 v92, 0xbfb8aa3b, v92
	v_add_f32_e32 v93, v93, v93
	v_exp_f32_e32 v92, v92
	v_mul_f32_e32 v93, 0xbfb8aa3b, v93
	v_exp_f32_e32 v101, v93
	v_add_f32_e32 v91, 1.0, v91
	v_rcp_f32_e32 v93, v91
	v_add_f32_e32 v91, 1.0, v92
	v_rcp_f32_e32 v106, v91
	v_add_f32_e32 v91, 1.0, v101
	v_mul_f32_e32 v92, 0x3d372713, v96
	v_mul_f32_e32 v101, 0x3d372713, v94
	v_mul_f32_e32 v92, v96, v92
	v_mul_f32_e32 v101, v94, v101
	v_fma_f32 v92, v96, v92, v96
	v_fma_f32 v101, v94, v101, v94
	v_mul_f32_e32 v92, 0x3f4c422a, v92
	v_mul_f32_e32 v101, 0x3f4c422a, v101
	v_add_f32_e32 v92, v92, v92
	v_add_f32_e32 v101, v101, v101
	v_mul_f32_e32 v92, 0xbfb8aa3b, v92
	v_mul_f32_e32 v101, 0xbfb8aa3b, v101
	v_exp_f32_e32 v92, v92
	v_exp_f32_e32 v101, v101
	v_rcp_f32_e32 v109, v91
	v_mul_f32_e32 v90, 0x3d372713, v104
	v_add_f32_e32 v91, 1.0, v92
	v_add_f32_e32 v92, 1.0, v101
	v_mul_f32_e32 v101, 0x3d372713, v97
	v_mul_f32_e32 v101, v97, v101
	v_mul_f32_e32 v107, 0x3d372713, v95
	v_mul_f32_e32 v90, v104, v90
	v_fma_f32 v101, v97, v101, v97
	v_mul_f32_e32 v107, v95, v107
	v_fma_f32 v90, v104, v90, v104
	v_mul_f32_e32 v101, 0x3f4c422a, v101
	v_fma_f32 v107, v95, v107, v95
	v_mul_f32_e32 v90, 0x3f4c422a, v90
	v_add_f32_e32 v101, v101, v101
	v_mul_f32_e32 v107, 0x3f4c422a, v107
	v_add_f32_e32 v90, v90, v90
	v_mul_f32_e32 v101, 0xbfb8aa3b, v101
	v_add_f32_e32 v107, v107, v107
	v_mul_f32_e32 v90, 0xbfb8aa3b, v90
	v_exp_f32_e32 v101, v101
	v_mul_f32_e32 v107, 0xbfb8aa3b, v107
	v_exp_f32_e32 v90, v90
	v_exp_f32_e32 v108, v107
	v_add_f32_e32 v101, 1.0, v101
	v_rcp_f32_e32 v107, v101
	v_add_f32_e32 v90, 1.0, v90
	v_add_f32_e32 v101, 1.0, v108
	v_rcp_f32_e32 v90, v90
	v_rcp_f32_e32 v91, v91
	v_rcp_f32_e32 v108, v101
	v_rcp_f32_e32 v92, v92
	v_mov_b32_e32 v111, v96
	v_mov_b32_e32 v96, v105
	v_mov_b32_e32 v110, v104
	v_pk_mul_f32 v[96:97], v[96:97], v[106:107]
	v_mov_b32_e32 v107, v102
	v_mov_b32_e32 v102, v95
	v_pk_mul_f32 v[90:91], v[110:111], v[90:91]
	v_pk_mul_f32 v[104:105], v[96:97], v[96:97]
	v_mov_b32_e32 v106, v94
	v_pk_mul_f32 v[108:109], v[102:103], v[108:109]
	v_pk_fma_f32 v[104:105], v[90:91], v[90:91], v[104:105]
	v_pk_mul_f32 v[92:93], v[106:107], v[92:93]
	v_pk_mul_f32 v[94:95], v[108:109], v[108:109]
	v_add_f32_e32 v101, v104, v105
	v_pk_fma_f32 v[94:95], v[92:93], v[92:93], v[94:95]
	v_mov_b32_e32 v104, v90
	v_add_f32_e32 v95, v95, v101
	v_add_f32_e32 v94, v94, v95
	v_cndmask_b32_e64 v106, 0, v94, s[10:11]
	v_mov_b32_e32 v105, v96
	v_mov_b32_e32 v96, v91
	v_mov_b32_e32 v102, v93
	v_mov_b32_e32 v103, v109
	v_mov_b32_e32 v94, v92
	v_mov_b32_e32 v95, v108

; __device__ __forceinline__ float sigm(float x) { return __builtin_amdgcn_rcpf(1.f + __builtin_amdgcn_exp2f(-1.4426950408889634f * x)); }
; __device__ __forceinline__ float gelu_t(float x) { const float u = 0.7978845608028654f * (x + 0.044715f * x * x * x); return x * sigm(2.f * u); }
; __device__ __forceinline__ u32x4 pack8(f32x4 v0, f32x4 v1) { u32x4 w; w.x = cvt_pk_bf16(v0[0], v0[1]); w.y = cvt_pk_bf16(v0[2], v0[3]); w.z = cvt_pk_bf16(v1[0], v1[1]); w.w = cvt_pk_bf16(v1[2], v1[3]); return w; }
; template <class T> __device__ __forceinline__ void est(T* p, T v) { if constexpr (MK_EPI_NT != 0) __builtin_nontemporal_store(v, p); else *p = v; }
; __device__ __forceinline__ unsigned pk4_u8(f32x4 v) { return q8(v[0]) | (q8(v[1]) << 8) | (q8(v[2]) << 16) | (q8(v[3]) << 24); }
; __device__ __forceinline__ float sum8sq(f32x4 a, f32x4 b) { return (a[0] * a[0] + a[1] * a[1]) + (a[2] * a[2] + a[3] * a[3]) + (b[0] * b[0] + b[1] * b[1]) + (b[2] * b[2] + b[3] * b[3]); }
; __device__ __forceinline__ float ss_val(const ss_t* ss, int row) { return (float)ss[row] * (1.f / 16777216.f); }
;     __device__ __forceinline__ void operator()(AccT acc, const Unit& u, int wr, int wc, int fr, int fq) const {
;     ...
;             for (int m = 0; m < 4; ++m) { const int row = row0 + ai * 128 + m * 16; const float r = rsqrtf(ss_val(ss, row) * (1.0f / DM) + EPS); bf16_t* rp = O + (size_t)row * NIN + col0; float sq = 0.f;
; #pragma unroll
;                 for (int bj = 0; bj < 2; ++bj) { f32x4 v0 = acc[ai][bj][m][0] * r, v1 = acc[ai][bj][m][1] * r;
;                     if (type == 1 || type == 2) {
; #pragma unroll
;                         for (int j = 0; j < 4; ++j) { v0[j] = gelu_t(v0[j]); v1[j] = gelu_t(v1[j]); }
;                         if (type == 2) sq += sum8sq(v0, v1); }
;                     if (type == 3) {
; #pragma unroll
;                         for (int j = 0; j < 4; ++j) { v0[j] = sigm(v0[j]); v1[j] = sigm(v1[j]); }
;                         est((u32x2*)(G8 + (size_t)row * (NIN - C_G) + (col0 - C_G) + bj * 128), (u32x2)(u32x2){pk4_u8(v0), pk4_u8(v1)}); }
;                     else est((u32x4*)(rp + bj * 128), (u32x4)pack8(v0, v1)); }
;                 if (type == 2) row_atomic(ssv, row, sq, fq); }
.LBB0_437:
	v_or_b32_e32 v82, 48, v146
	s_waitcnt lgkmcnt(0)
	v_ashrrev_i32_e32 v83, 31, v82
	v_lshl_add_u64 v[84:85], v[82:83], 3, s[26:27]
	s_nop 0
	s_and_b64 vcc, exec, s[12:13]
	v_mov_b32_e32 v90, 0
	s_waitcnt vmcnt(3)
	v_mov_b32_e32 v84, v254
	v_mov_b32_e32 v85, v255
	global_load_dwordx2 v[254:255], v[148:149], off offset:1408
	v_ffbh_u32_e32 v86, v85
	v_min_u32_e32 v86, 32, v86
	v_lshlrev_b64 v[84:85], v86, v[84:85]
	v_min_u32_e32 v84, 1, v84
	v_or_b32_e32 v84, v85, v84
	v_cvt_f32_u32_e32 v84, v84
	v_sub_u32_e32 v85, 32, v86
	v_ldexp_f32 v84, v84, v85
	v_mul_f32_e32 v84, 0x33800000, v84
	v_fmamk_f32 v84, v84, 0x3a000000, v164
	v_mul_f32_e32 v85, 0x4b800000, v84
	v_cmp_gt_f32_e64 s[16:17], s89, v84
	s_nop 1
	v_cndmask_b32_e64 v84, v84, v85, s[16:17]
	v_rsq_f32_e32 v84, v84
	s_nop 0
	v_mul_f32_e32 v85, 0x45800000, v84
	v_cndmask_b32_e64 v84, v84, v85, s[16:17]
	v_pk_mul_f32 v[80:81], v[80:81], v[84:85] op_sel_hi:[1,0]
	v_pk_mul_f32 v[88:89], v[78:79], v[84:85] op_sel_hi:[1,0]
	v_pk_mul_f32 v[78:79], v[76:77], v[84:85] op_sel_hi:[1,0]
	v_pk_mul_f32 v[86:87], v[74:75], v[84:85] op_sel_hi:[1,0]
	s_cbranch_vccnz .LBB0_439
	v_mul_f32_e32 v75, 0x3d372713, v86
	v_mul_f32_e32 v75, v86, v75
	v_mul_f32_e32 v76, 0x3d372713, v89
	v_fma_f32 v75, v86, v75, v86
	v_mul_f32_e32 v76, v89, v76
	v_mul_f32_e32 v77, 0x3d372713, v87
	v_mul_f32_e32 v75, 0x3f4c422a, v75
	v_fma_f32 v76, v89, v76, v89
	v_mul_f32_e32 v77, v87, v77
	v_add_f32_e32 v75, v75, v75
	v_mul_f32_e32 v76, 0x3f4c422a, v76
	v_fma_f32 v77, v87, v77, v87
	v_mul_f32_e32 v75, 0xbfb8aa3b, v75
	v_add_f32_e32 v76, v76, v76
	v_mul_f32_e32 v77, 0x3f4c422a, v77
	v_exp_f32_e32 v75, v75
	v_mul_f32_e32 v76, 0xbfb8aa3b, v76
	v_add_f32_e32 v77, v77, v77
	v_exp_f32_e32 v76, v76
	v_mul_f32_e32 v77, 0xbfb8aa3b, v77
	v_exp_f32_e32 v85, v77
	v_add_f32_e32 v75, 1.0, v75
	v_rcp_f32_e32 v77, v75
	v_add_f32_e32 v75, 1.0, v76
	v_rcp_f32_e32 v90, v75
	v_add_f32_e32 v75, 1.0, v85
	v_mul_f32_e32 v76, 0x3d372713, v80
	v_mul_f32_e32 v85, 0x3d372713, v78
	v_mul_f32_e32 v76, v80, v76
	v_mul_f32_e32 v85, v78, v85
	v_fma_f32 v76, v80, v76, v80
	v_fma_f32 v85, v78, v85, v78
	v_mul_f32_e32 v76, 0x3f4c422a, v76
	v_mul_f32_e32 v85, 0x3f4c422a, v85
	v_add_f32_e32 v76, v76, v76
	v_add_f32_e32 v85, v85, v85
	v_mul_f32_e32 v76, 0xbfb8aa3b, v76
	v_mul_f32_e32 v85, 0xbfb8aa3b, v85
	v_exp_f32_e32 v76, v76
	v_exp_f32_e32 v85, v85
	v_rcp_f32_e32 v93, v75
	v_mul_f32_e32 v74, 0x3d372713, v88
	v_add_f32_e32 v75, 1.0, v76
	v_add_f32_e32 v76, 1.0, v85
	v_mul_f32_e32 v85, 0x3d372713, v81
	v_mul_f32_e32 v85, v81, v85
	v_mul_f32_e32 v91, 0x3d372713, v79
	v_mul_f32_e32 v74, v88, v74
	v_fma_f32 v85, v81, v85, v81
	v_mul_f32_e32 v91, v79, v91
	v_fma_f32 v74, v88, v74, v88
	v_mul_f32_e32 v85, 0x3f4c422a, v85
	v_fma_f32 v91, v79, v91, v79
	v_mul_f32_e32 v74, 0x3f4c422a, v74
	v_add_f32_e32 v85, v85, v85
	v_mul_f32_e32 v91, 0x3f4c422a, v91
	v_add_f32_e32 v74, v74, v74
	v_mul_f32_e32 v85, 0xbfb8aa3b, v85
	v_add_f32_e32 v91, v91, v91
	v_mul_f32_e32 v74, 0xbfb8aa3b, v74
	v_exp_f32_e32 v85, v85
	v_mul_f32_e32 v91, 0xbfb8aa3b, v91
	v_exp_f32_e32 v74, v74
	v_exp_f32_e32 v92, v91
	v_add_f32_e32 v85, 1.0, v85
	v_rcp_f32_e32 v91, v85
	v_add_f32_e32 v74, 1.0, v74
	v_add_f32_e32 v85, 1.0, v92
	v_rcp_f32_e32 v74, v74
	v_rcp_f32_e32 v75, v75
	v_rcp_f32_e32 v92, v85
	v_rcp_f32_e32 v76, v76
	v_mov_b32_e32 v95, v80
	v_mov_b32_e32 v80, v89
	v_mov_b32_e32 v94, v88
	v_pk_mul_f32 v[80:81], v[80:81], v[90:91]
	v_mov_b32_e32 v91, v86
	v_mov_b32_e32 v86, v79
	v_pk_mul_f32 v[74:75], v[94:95], v[74:75]
	v_pk_mul_f32 v[88:89], v[80:81], v[80:81]
	v_mov_b32_e32 v90, v78
	v_pk_mul_f32 v[92:93], v[86:87], v[92:93]
	v_pk_fma_f32 v[88:89], v[74:75], v[74:75], v[88:89]
	v_pk_mul_f32 v[76:77], v[90:91], v[76:77]
	v_pk_mul_f32 v[78:79], v[92:93], v[92:93]
	v_add_f32_e32 v85, v88, v89
	v_pk_fma_f32 v[78:79], v[76:77], v[76:77], v[78:79]
	v_mov_b32_e32 v88, v74
	v_add_f32_e32 v79, v79, v85
	v_add_f32_e32 v78, v78, v79
	v_cndmask_b32_e64 v90, 0, v78, s[10:11]
	v_mov_b32_e32 v89, v80
	v_mov_b32_e32 v80, v75
	v_mov_b32_e32 v86, v77
	v_mov_b32_e32 v87, v93
	v_mov_b32_e32 v78, v76
	v_mov_b32_e32 v79, v92

; __device__ __forceinline__ float sigm(float x) { return __builtin_amdgcn_rcpf(1.f + __builtin_amdgcn_exp2f(-1.4426950408889634f * x)); }
; __device__ __forceinline__ float gelu_t(float x) { const float u = 0.7978845608028654f * (x + 0.044715f * x * x * x); return x * sigm(2.f * u); }
; __device__ __forceinline__ u32x4 pack8(f32x4 v0, f32x4 v1) { u32x4 w; w.x = cvt_pk_bf16(v0[0], v0[1]); w.y = cvt_pk_bf16(v0[2], v0[3]); w.z = cvt_pk_bf16(v1[0], v1[1]); w.w = cvt_pk_bf16(v1[2], v1[3]); return w; }
; template <class T> __device__ __forceinline__ void est(T* p, T v) { if constexpr (MK_EPI_NT != 0) __builtin_nontemporal_store(v, p); else *p = v; }
; __device__ __forceinline__ unsigned pk4_u8(f32x4 v) { return q8(v[0]) | (q8(v[1]) << 8) | (q8(v[2]) << 16) | (q8(v[3]) << 24); }
; __device__ __forceinline__ float sum8sq(f32x4 a, f32x4 b) { return (a[0] * a[0] + a[1] * a[1]) + (a[2] * a[2] + a[3] * a[3]) + (b[0] * b[0] + b[1] * b[1]) + (b[2] * b[2] + b[3] * b[3]); }
; __device__ __forceinline__ float ss_val(const ss_t* ss, int row) { return (float)ss[row] * (1.f / 16777216.f); }
;     __device__ __forceinline__ void operator()(AccT acc, const Unit& u, int wr, int wc, int fr, int fq) const {
;     ...
;             for (int m = 0; m < 4; ++m) { const int row = row0 + ai * 128 + m * 16; const float r = rsqrtf(ss_val(ss, row) * (1.0f / DM) + EPS); bf16_t* rp = O + (size_t)row * NIN + col0; float sq = 0.f;
; #pragma unroll
;                 for (int bj = 0; bj < 2; ++bj) { f32x4 v0 = acc[ai][bj][m][0] * r, v1 = acc[ai][bj][m][1] * r;
;                     if (type == 1 || type == 2) {
; #pragma unroll
;                         for (int j = 0; j < 4; ++j) { v0[j] = gelu_t(v0[j]); v1[j] = gelu_t(v1[j]); }
;                         if (type == 2) sq += sum8sq(v0, v1); }
;                     if (type == 3) {
; #pragma unroll
;                         for (int j = 0; j < 4; ++j) { v0[j] = sigm(v0[j]); v1[j] = sigm(v1[j]); }
;                         est((u32x2*)(G8 + (size_t)row * (NIN - C_G) + (col0 - C_G) + bj * 128), (u32x2)(u32x2){pk4_u8(v0), pk4_u8(v1)}); }
;                     else est((u32x4*)(rp + bj * 128), (u32x4)pack8(v0, v1)); }
;                 if (type == 2) row_atomic(ssv, row, sq, fq); }
.LBB0_455:
	s_waitcnt lgkmcnt(0)
	s_nop 0
	s_and_b64 vcc, exec, s[12:13]
	s_waitcnt vmcnt(3)
	v_mov_b32_e32 v66, v248
	v_mov_b32_e32 v67, v249
	v_ffbh_u32_e32 v68, v67
	v_min_u32_e32 v68, 32, v68
	v_lshlrev_b64 v[66:67], v68, v[66:67]
	v_min_u32_e32 v66, 1, v66
	v_or_b32_e32 v66, v67, v66
	v_cvt_f32_u32_e32 v66, v66
	v_sub_u32_e32 v67, 32, v68
	v_ldexp_f32 v66, v66, v67
	v_mul_f32_e32 v66, 0x33800000, v66
	v_fmamk_f32 v66, v66, 0x3a000000, v164
	v_mul_f32_e32 v67, 0x4b800000, v66
	v_cmp_gt_f32_e64 s[16:17], s89, v66
	s_nop 1
	v_cndmask_b32_e64 v66, v66, v67, s[16:17]
	v_rsq_f32_e32 v66, v66
	s_nop 0
	v_mul_f32_e32 v67, 0x45800000, v66
	v_cndmask_b32_e64 v66, v66, v67, s[16:17]
	v_pk_mul_f32 v[64:65], v[64:65], v[66:67] op_sel_hi:[1,0]
	v_pk_mul_f32 v[72:73], v[62:63], v[66:67] op_sel_hi:[1,0]
	v_pk_mul_f32 v[68:69], v[60:61], v[66:67] op_sel_hi:[1,0]
	v_pk_mul_f32 v[70:71], v[58:59], v[66:67] op_sel_hi:[1,0]
	v_mov_b32_e32 v59, 0
	s_cbranch_vccnz .LBB0_457
	v_mul_f32_e32 v59, 0x3d372713, v70
	v_mul_f32_e32 v59, v70, v59
	v_mul_f32_e32 v60, 0x3d372713, v73
	v_fma_f32 v59, v70, v59, v70
	v_mul_f32_e32 v60, v73, v60
	v_mul_f32_e32 v61, 0x3d372713, v71
	v_mul_f32_e32 v59, 0x3f4c422a, v59
	v_fma_f32 v60, v73, v60, v73
	v_mul_f32_e32 v61, v71, v61
	v_add_f32_e32 v59, v59, v59
	v_mul_f32_e32 v60, 0x3f4c422a, v60
	v_fma_f32 v61, v71, v61, v71
	v_mul_f32_e32 v59, 0xbfb8aa3b, v59
	v_add_f32_e32 v60, v60, v60
	v_mul_f32_e32 v61, 0x3f4c422a, v61
	v_exp_f32_e32 v59, v59
	v_mul_f32_e32 v60, 0xbfb8aa3b, v60
	v_add_f32_e32 v61, v61, v61
	v_exp_f32_e32 v60, v60
	v_mul_f32_e32 v61, 0xbfb8aa3b, v61
	v_exp_f32_e32 v63, v61
	v_add_f32_e32 v59, 1.0, v59
	v_rcp_f32_e32 v61, v59
	v_add_f32_e32 v59, 1.0, v60
	v_rcp_f32_e32 v62, v59
	v_add_f32_e32 v59, 1.0, v63
	v_mul_f32_e32 v60, 0x3d372713, v64
	v_mul_f32_e32 v63, 0x3d372713, v68
	v_mul_f32_e32 v60, v64, v60
	v_mul_f32_e32 v63, v68, v63
	v_fma_f32 v60, v64, v60, v64
	v_fma_f32 v63, v68, v63, v68
	v_mul_f32_e32 v60, 0x3f4c422a, v60
	v_mul_f32_e32 v63, 0x3f4c422a, v63
	v_add_f32_e32 v60, v60, v60
	v_add_f32_e32 v63, v63, v63
	v_mul_f32_e32 v60, 0xbfb8aa3b, v60
	v_mul_f32_e32 v63, 0xbfb8aa3b, v63
	v_exp_f32_e32 v60, v60
	v_exp_f32_e32 v63, v63
	v_rcp_f32_e32 v75, v59
	v_mul_f32_e32 v58, 0x3d372713, v72
	v_add_f32_e32 v59, 1.0, v60
	v_add_f32_e32 v60, 1.0, v63
	v_mul_f32_e32 v63, 0x3d372713, v65
	v_mul_f32_e32 v63, v65, v63
	v_mul_f32_e32 v67, 0x3d372713, v69
	v_mul_f32_e32 v58, v72, v58
	v_fma_f32 v63, v65, v63, v65
	v_mul_f32_e32 v67, v69, v67
	v_fma_f32 v58, v72, v58, v72
	v_mul_f32_e32 v63, 0x3f4c422a, v63
	v_fma_f32 v67, v69, v67, v69
	v_mul_f32_e32 v58, 0x3f4c422a, v58
	v_add_f32_e32 v63, v63, v63
	v_mul_f32_e32 v67, 0x3f4c422a, v67
	v_add_f32_e32 v58, v58, v58
	v_mul_f32_e32 v63, 0xbfb8aa3b, v63
	v_add_f32_e32 v67, v67, v67
	v_mul_f32_e32 v58, 0xbfb8aa3b, v58
	v_exp_f32_e32 v63, v63
	v_mul_f32_e32 v67, 0xbfb8aa3b, v67
	v_exp_f32_e32 v58, v58
	v_exp_f32_e32 v67, v67
	v_add_f32_e32 v63, 1.0, v63
	v_rcp_f32_e32 v63, v63
	v_add_f32_e32 v58, 1.0, v58
	v_add_f32_e32 v67, 1.0, v67
	v_rcp_f32_e32 v58, v58
	v_rcp_f32_e32 v59, v59
	v_rcp_f32_e32 v60, v60
	v_rcp_f32_e32 v74, v67
	v_mov_b32_e32 v77, v64
	v_mov_b32_e32 v64, v73
	v_mov_b32_e32 v76, v72
	v_pk_mul_f32 v[64:65], v[64:65], v[62:63]
	v_mov_b32_e32 v62, v68
	v_mov_b32_e32 v63, v70
	v_mov_b32_e32 v70, v69
	v_pk_mul_f32 v[76:77], v[76:77], v[58:59]
	v_pk_mul_f32 v[58:59], v[64:65], v[64:65]
	v_pk_mul_f32 v[60:61], v[62:63], v[60:61]
	v_pk_mul_f32 v[62:63], v[70:71], v[74:75]
	v_pk_fma_f32 v[58:59], v[76:77], v[76:77], v[58:59]
	v_pk_mul_f32 v[68:69], v[62:63], v[62:63]
	v_add_f32_e32 v58, v58, v59
	v_pk_fma_f32 v[68:69], v[60:61], v[60:61], v[68:69]
	v_mov_b32_e32 v72, v76
	v_add_f32_e32 v58, v69, v58
	v_add_f32_e32 v58, v68, v58
	v_cndmask_b32_e64 v59, 0, v58, s[10:11]
	v_mov_b32_e32 v73, v64
	v_mov_b32_e32 v64, v77
	v_mov_b32_e32 v70, v61
	v_mov_b32_e32 v71, v63
	v_mov_b32_e32 v68, v60
	v_mov_b32_e32 v69, v62

; __device__ __forceinline__ float sigm(float x) { return __builtin_amdgcn_rcpf(1.f + __builtin_amdgcn_exp2f(-1.4426950408889634f * x)); }
; __device__ __forceinline__ float gelu_t(float x) { const float u = 0.7978845608028654f * (x + 0.044715f * x * x * x); return x * sigm(2.f * u); }
; __device__ __forceinline__ u32x4 pack8(f32x4 v0, f32x4 v1) { u32x4 w; w.x = cvt_pk_bf16(v0[0], v0[1]); w.y = cvt_pk_bf16(v0[2], v0[3]); w.z = cvt_pk_bf16(v1[0], v1[1]); w.w = cvt_pk_bf16(v1[2], v1[3]); return w; }
; template <class T> __device__ __forceinline__ void est(T* p, T v) { if constexpr (MK_EPI_NT != 0) __builtin_nontemporal_store(v, p); else *p = v; }
; __device__ __forceinline__ unsigned pk4_u8(f32x4 v) { return q8(v[0]) | (q8(v[1]) << 8) | (q8(v[2]) << 16) | (q8(v[3]) << 24); }
; __device__ __forceinline__ float sum8sq(f32x4 a, f32x4 b) { return (a[0] * a[0] + a[1] * a[1]) + (a[2] * a[2] + a[3] * a[3]) + (b[0] * b[0] + b[1] * b[1]) + (b[2] * b[2] + b[3] * b[3]); }
; __device__ __forceinline__ float ss_val(const ss_t* ss, int row) { return (float)ss[row] * (1.f / 16777216.f); }
;     __device__ __forceinline__ void operator()(AccT acc, const Unit& u, int wr, int wc, int fr, int fq) const {
;     ...
;             for (int m = 0; m < 4; ++m) { const int row = row0 + ai * 128 + m * 16; const float r = rsqrtf(ss_val(ss, row) * (1.0f / DM) + EPS); bf16_t* rp = O + (size_t)row * NIN + col0; float sq = 0.f;
; #pragma unroll
;                 for (int bj = 0; bj < 2; ++bj) { f32x4 v0 = acc[ai][bj][m][0] * r, v1 = acc[ai][bj][m][1] * r;
;                     if (type == 1 || type == 2) {
; #pragma unroll
;                         for (int j = 0; j < 4; ++j) { v0[j] = gelu_t(v0[j]); v1[j] = gelu_t(v1[j]); }
;                         if (type == 2) sq += sum8sq(v0, v1); }
;                     if (type == 3) {
; #pragma unroll
;                         for (int j = 0; j < 4; ++j) { v0[j] = sigm(v0[j]); v1[j] = sigm(v1[j]); }
;                         est((u32x2*)(G8 + (size_t)row * (NIN - C_G) + (col0 - C_G) + bj * 128), (u32x2)(u32x2){pk4_u8(v0), pk4_u8(v1)}); }
;                     else est((u32x4*)(rp + bj * 128), (u32x4)pack8(v0, v1)); }
;                 if (type == 2) row_atomic(ssv, row, sq, fq); }
.LBB0_473:
	s_waitcnt lgkmcnt(0)
	s_nop 0
	s_and_b64 vcc, exec, s[12:13]
	s_waitcnt vmcnt(2)
	v_mov_b32_e32 v50, v250
	v_mov_b32_e32 v51, v251
	v_ffbh_u32_e32 v52, v51
	v_min_u32_e32 v52, 32, v52
	v_lshlrev_b64 v[50:51], v52, v[50:51]
	v_min_u32_e32 v50, 1, v50
	v_or_b32_e32 v50, v51, v50
	v_cvt_f32_u32_e32 v50, v50
	v_sub_u32_e32 v51, 32, v52
	v_ldexp_f32 v50, v50, v51
	v_mul_f32_e32 v50, 0x33800000, v50
	v_fmamk_f32 v50, v50, 0x3a000000, v164
	v_mul_f32_e32 v51, 0x4b800000, v50
	v_cmp_gt_f32_e64 s[16:17], s89, v50
	s_nop 1
	v_cndmask_b32_e64 v50, v50, v51, s[16:17]
	v_rsq_f32_e32 v50, v50
	s_nop 0
	v_mul_f32_e32 v51, 0x45800000, v50
	v_cndmask_b32_e64 v50, v50, v51, s[16:17]
	v_pk_mul_f32 v[48:49], v[48:49], v[50:51] op_sel_hi:[1,0]
	v_pk_mul_f32 v[56:57], v[46:47], v[50:51] op_sel_hi:[1,0]
	v_pk_mul_f32 v[52:53], v[44:45], v[50:51] op_sel_hi:[1,0]
	v_pk_mul_f32 v[54:55], v[42:43], v[50:51] op_sel_hi:[1,0]
	v_mov_b32_e32 v43, 0
	s_cbranch_vccnz .LBB0_475
	v_mul_f32_e32 v43, 0x3d372713, v54
	v_mul_f32_e32 v43, v54, v43
	v_mul_f32_e32 v44, 0x3d372713, v57
	v_fma_f32 v43, v54, v43, v54
	v_mul_f32_e32 v44, v57, v44
	v_mul_f32_e32 v45, 0x3d372713, v55
	v_mul_f32_e32 v43, 0x3f4c422a, v43
	v_fma_f32 v44, v57, v44, v57
	v_mul_f32_e32 v45, v55, v45
	v_add_f32_e32 v43, v43, v43
	v_mul_f32_e32 v44, 0x3f4c422a, v44
	v_fma_f32 v45, v55, v45, v55
	v_mul_f32_e32 v43, 0xbfb8aa3b, v43
	v_add_f32_e32 v44, v44, v44
	v_mul_f32_e32 v45, 0x3f4c422a, v45
	v_exp_f32_e32 v43, v43
	v_mul_f32_e32 v44, 0xbfb8aa3b, v44
	v_add_f32_e32 v45, v45, v45
	v_exp_f32_e32 v44, v44
	v_mul_f32_e32 v45, 0xbfb8aa3b, v45
	v_exp_f32_e32 v47, v45
	v_add_f32_e32 v43, 1.0, v43
	v_rcp_f32_e32 v45, v43
	v_add_f32_e32 v43, 1.0, v44
	v_rcp_f32_e32 v46, v43
	v_add_f32_e32 v43, 1.0, v47
	v_mul_f32_e32 v44, 0x3d372713, v48
	v_mul_f32_e32 v47, 0x3d372713, v52
	v_mul_f32_e32 v44, v48, v44
	v_mul_f32_e32 v47, v52, v47
	v_fma_f32 v44, v48, v44, v48
	v_fma_f32 v47, v52, v47, v52
	v_mul_f32_e32 v44, 0x3f4c422a, v44
	v_mul_f32_e32 v47, 0x3f4c422a, v47
	v_add_f32_e32 v44, v44, v44
	v_add_f32_e32 v47, v47, v47
	v_mul_f32_e32 v44, 0xbfb8aa3b, v44
	v_mul_f32_e32 v47, 0xbfb8aa3b, v47
	v_exp_f32_e32 v44, v44
	v_exp_f32_e32 v47, v47
	v_rcp_f32_e32 v59, v43
	v_mul_f32_e32 v42, 0x3d372713, v56
	v_add_f32_e32 v43, 1.0, v44
	v_add_f32_e32 v44, 1.0, v47
	v_mul_f32_e32 v47, 0x3d372713, v49
	v_mul_f32_e32 v47, v49, v47
	v_mul_f32_e32 v51, 0x3d372713, v53
	v_mul_f32_e32 v42, v56, v42
	v_fma_f32 v47, v49, v47, v49
	v_mul_f32_e32 v51, v53, v51
	v_fma_f32 v42, v56, v42, v56
	v_mul_f32_e32 v47, 0x3f4c422a, v47
	v_fma_f32 v51, v53, v51, v53
	v_mul_f32_e32 v42, 0x3f4c422a, v42
	v_add_f32_e32 v47, v47, v47
	v_mul_f32_e32 v51, 0x3f4c422a, v51
	v_add_f32_e32 v42, v42, v42
	v_mul_f32_e32 v47, 0xbfb8aa3b, v47
	v_add_f32_e32 v51, v51, v51
	v_mul_f32_e32 v42, 0xbfb8aa3b, v42
	v_exp_f32_e32 v47, v47
	v_mul_f32_e32 v51, 0xbfb8aa3b, v51
	v_exp_f32_e32 v42, v42
	v_exp_f32_e32 v51, v51
	v_add_f32_e32 v47, 1.0, v47
	v_rcp_f32_e32 v47, v47
	v_add_f32_e32 v42, 1.0, v42
	v_add_f32_e32 v51, 1.0, v51
	v_rcp_f32_e32 v42, v42
	v_rcp_f32_e32 v43, v43
	v_rcp_f32_e32 v44, v44
	v_rcp_f32_e32 v58, v51
	v_mov_b32_e32 v61, v48
	v_mov_b32_e32 v48, v57
	v_mov_b32_e32 v60, v56
	v_pk_mul_f32 v[48:49], v[48:49], v[46:47]
	v_mov_b32_e32 v46, v52
	v_mov_b32_e32 v47, v54
	v_mov_b32_e32 v54, v53
	v_pk_mul_f32 v[60:61], v[60:61], v[42:43]
	v_pk_mul_f32 v[42:43], v[48:49], v[48:49]
	v_pk_mul_f32 v[44:45], v[46:47], v[44:45]
	v_pk_mul_f32 v[46:47], v[54:55], v[58:59]
	v_pk_fma_f32 v[42:43], v[60:61], v[60:61], v[42:43]
	v_pk_mul_f32 v[52:53], v[46:47], v[46:47]
	v_add_f32_e32 v42, v42, v43
	v_pk_fma_f32 v[52:53], v[44:45], v[44:45], v[52:53]
	v_mov_b32_e32 v56, v60
	v_add_f32_e32 v42, v53, v42
	v_add_f32_e32 v42, v52, v42
	v_cndmask_b32_e64 v43, 0, v42, s[10:11]
	v_mov_b32_e32 v57, v48
	v_mov_b32_e32 v48, v61
	v_mov_b32_e32 v54, v45
	v_mov_b32_e32 v55, v47
	v_mov_b32_e32 v52, v44
	v_mov_b32_e32 v53, v46

; __device__ __forceinline__ float sigm(float x) { return __builtin_amdgcn_rcpf(1.f + __builtin_amdgcn_exp2f(-1.4426950408889634f * x)); }
; __device__ __forceinline__ float gelu_t(float x) { const float u = 0.7978845608028654f * (x + 0.044715f * x * x * x); return x * sigm(2.f * u); }
; __device__ __forceinline__ u32x4 pack8(f32x4 v0, f32x4 v1) { u32x4 w; w.x = cvt_pk_bf16(v0[0], v0[1]); w.y = cvt_pk_bf16(v0[2], v0[3]); w.z = cvt_pk_bf16(v1[0], v1[1]); w.w = cvt_pk_bf16(v1[2], v1[3]); return w; }
; template <class T> __device__ __forceinline__ void est(T* p, T v) { if constexpr (MK_EPI_NT != 0) __builtin_nontemporal_store(v, p); else *p = v; }
; __device__ __forceinline__ unsigned pk4_u8(f32x4 v) { return q8(v[0]) | (q8(v[1]) << 8) | (q8(v[2]) << 16) | (q8(v[3]) << 24); }
; __device__ __forceinline__ float sum8sq(f32x4 a, f32x4 b) { return (a[0] * a[0] + a[1] * a[1]) + (a[2] * a[2] + a[3] * a[3]) + (b[0] * b[0] + b[1] * b[1]) + (b[2] * b[2] + b[3] * b[3]); }
; __device__ __forceinline__ float ss_val(const ss_t* ss, int row) { return (float)ss[row] * (1.f / 16777216.f); }
;     __device__ __forceinline__ void operator()(AccT acc, const Unit& u, int wr, int wc, int fr, int fq) const {
;     ...
;             for (int m = 0; m < 4; ++m) { const int row = row0 + ai * 128 + m * 16; const float r = rsqrtf(ss_val(ss, row) * (1.0f / DM) + EPS); bf16_t* rp = O + (size_t)row * NIN + col0; float sq = 0.f;
; #pragma unroll
;                 for (int bj = 0; bj < 2; ++bj) { f32x4 v0 = acc[ai][bj][m][0] * r, v1 = acc[ai][bj][m][1] * r;
;                     if (type == 1 || type == 2) {
; #pragma unroll
;                         for (int j = 0; j < 4; ++j) { v0[j] = gelu_t(v0[j]); v1[j] = gelu_t(v1[j]); }
;                         if (type == 2) sq += sum8sq(v0, v1); }
;                     if (type == 3) {
; #pragma unroll
;                         for (int j = 0; j < 4; ++j) { v0[j] = sigm(v0[j]); v1[j] = sigm(v1[j]); }
;                         est((u32x2*)(G8 + (size_t)row * (NIN - C_G) + (col0 - C_G) + bj * 128), (u32x2)(u32x2){pk4_u8(v0), pk4_u8(v1)}); }
;                     else est((u32x4*)(rp + bj * 128), (u32x4)pack8(v0, v1)); }
;                 if (type == 2) row_atomic(ssv, row, sq, fq); }
.LBB0_491:
	s_waitcnt lgkmcnt(0)
	s_nop 0
	s_and_b64 vcc, exec, s[12:13]
	s_waitcnt vmcnt(1)
	v_mov_b32_e32 v34, v252
	v_mov_b32_e32 v35, v253
	v_ffbh_u32_e32 v36, v35
	v_min_u32_e32 v36, 32, v36
	v_lshlrev_b64 v[34:35], v36, v[34:35]
	v_min_u32_e32 v34, 1, v34
	v_or_b32_e32 v34, v35, v34
	v_cvt_f32_u32_e32 v34, v34
	v_sub_u32_e32 v35, 32, v36
	v_ldexp_f32 v34, v34, v35
	v_mul_f32_e32 v34, 0x33800000, v34
	v_fmamk_f32 v34, v34, 0x3a000000, v164
	v_mul_f32_e32 v35, 0x4b800000, v34
	v_cmp_gt_f32_e64 s[16:17], s89, v34
	s_nop 1
	v_cndmask_b32_e64 v34, v34, v35, s[16:17]
	v_rsq_f32_e32 v34, v34
	s_nop 0
	v_mul_f32_e32 v35, 0x45800000, v34
	v_cndmask_b32_e64 v34, v34, v35, s[16:17]
	v_pk_mul_f32 v[32:33], v[32:33], v[34:35] op_sel_hi:[1,0]
	v_pk_mul_f32 v[40:41], v[30:31], v[34:35] op_sel_hi:[1,0]
	v_pk_mul_f32 v[36:37], v[28:29], v[34:35] op_sel_hi:[1,0]
	v_pk_mul_f32 v[38:39], v[26:27], v[34:35] op_sel_hi:[1,0]
	v_mov_b32_e32 v27, 0
	s_cbranch_vccnz .LBB0_493
	v_mul_f32_e32 v27, 0x3d372713, v38
	v_mul_f32_e32 v27, v38, v27
	v_mul_f32_e32 v28, 0x3d372713, v41
	v_fma_f32 v27, v38, v27, v38
	v_mul_f32_e32 v28, v41, v28
	v_mul_f32_e32 v29, 0x3d372713, v39
	v_mul_f32_e32 v27, 0x3f4c422a, v27
	v_fma_f32 v28, v41, v28, v41
	v_mul_f32_e32 v29, v39, v29
	v_add_f32_e32 v27, v27, v27
	v_mul_f32_e32 v28, 0x3f4c422a, v28
	v_fma_f32 v29, v39, v29, v39
	v_mul_f32_e32 v27, 0xbfb8aa3b, v27
	v_add_f32_e32 v28, v28, v28
	v_mul_f32_e32 v29, 0x3f4c422a, v29
	v_exp_f32_e32 v27, v27
	v_mul_f32_e32 v28, 0xbfb8aa3b, v28
	v_add_f32_e32 v29, v29, v29
	v_exp_f32_e32 v28, v28
	v_mul_f32_e32 v29, 0xbfb8aa3b, v29
	v_exp_f32_e32 v31, v29
	v_add_f32_e32 v27, 1.0, v27
	v_rcp_f32_e32 v29, v27
	v_add_f32_e32 v27, 1.0, v28
	v_rcp_f32_e32 v30, v27
	v_add_f32_e32 v27, 1.0, v31
	v_mul_f32_e32 v28, 0x3d372713, v32
	v_mul_f32_e32 v31, 0x3d372713, v36
	v_mul_f32_e32 v28, v32, v28
	v_mul_f32_e32 v31, v36, v31
	v_fma_f32 v28, v32, v28, v32
	v_fma_f32 v31, v36, v31, v36
	v_mul_f32_e32 v28, 0x3f4c422a, v28
	v_mul_f32_e32 v31, 0x3f4c422a, v31
	v_add_f32_e32 v28, v28, v28
	v_add_f32_e32 v31, v31, v31
	v_mul_f32_e32 v28, 0xbfb8aa3b, v28
	v_mul_f32_e32 v31, 0xbfb8aa3b, v31
	v_exp_f32_e32 v28, v28
	v_exp_f32_e32 v31, v31
	v_rcp_f32_e32 v43, v27
	v_mul_f32_e32 v26, 0x3d372713, v40
	v_add_f32_e32 v27, 1.0, v28
	v_add_f32_e32 v28, 1.0, v31
	v_mul_f32_e32 v31, 0x3d372713, v33
	v_mul_f32_e32 v31, v33, v31
	v_mul_f32_e32 v35, 0x3d372713, v37
	v_mul_f32_e32 v26, v40, v26
	v_fma_f32 v31, v33, v31, v33
	v_mul_f32_e32 v35, v37, v35
	v_fma_f32 v26, v40, v26, v40
	v_mul_f32_e32 v31, 0x3f4c422a, v31
	v_fma_f32 v35, v37, v35, v37
	v_mul_f32_e32 v26, 0x3f4c422a, v26
	v_add_f32_e32 v31, v31, v31
	v_mul_f32_e32 v35, 0x3f4c422a, v35
	v_add_f32_e32 v26, v26, v26
	v_mul_f32_e32 v31, 0xbfb8aa3b, v31
	v_add_f32_e32 v35, v35, v35
	v_mul_f32_e32 v26, 0xbfb8aa3b, v26
	v_exp_f32_e32 v31, v31
	v_mul_f32_e32 v35, 0xbfb8aa3b, v35
	v_exp_f32_e32 v26, v26
	v_exp_f32_e32 v35, v35
	v_add_f32_e32 v31, 1.0, v31
	v_rcp_f32_e32 v31, v31
	v_add_f32_e32 v26, 1.0, v26
	v_add_f32_e32 v35, 1.0, v35
	v_rcp_f32_e32 v26, v26
	v_rcp_f32_e32 v27, v27
	v_rcp_f32_e32 v28, v28
	v_rcp_f32_e32 v42, v35
	v_mov_b32_e32 v45, v32
	v_mov_b32_e32 v32, v41
	v_mov_b32_e32 v44, v40
	v_pk_mul_f32 v[32:33], v[32:33], v[30:31]
	v_mov_b32_e32 v30, v36
	v_mov_b32_e32 v31, v38
	v_mov_b32_e32 v38, v37
	v_pk_mul_f32 v[44:45], v[44:45], v[26:27]
	v_pk_mul_f32 v[26:27], v[32:33], v[32:33]
	v_pk_mul_f32 v[28:29], v[30:31], v[28:29]
	v_pk_mul_f32 v[30:31], v[38:39], v[42:43]
	v_pk_fma_f32 v[26:27], v[44:45], v[44:45], v[26:27]
	v_pk_mul_f32 v[36:37], v[30:31], v[30:31]
	v_add_f32_e32 v26, v26, v27
	v_pk_fma_f32 v[36:37], v[28:29], v[28:29], v[36:37]
	v_mov_b32_e32 v40, v44
	v_add_f32_e32 v26, v37, v26
	v_add_f32_e32 v26, v36, v26
	v_cndmask_b32_e64 v27, 0, v26, s[10:11]
	v_mov_b32_e32 v41, v32
	v_mov_b32_e32 v32, v45
	v_mov_b32_e32 v38, v29
	v_mov_b32_e32 v39, v31
	v_mov_b32_e32 v36, v28
	v_mov_b32_e32 v37, v30

; __device__ __forceinline__ float sigm(float x) { return __builtin_amdgcn_rcpf(1.f + __builtin_amdgcn_exp2f(-1.4426950408889634f * x)); }
; __device__ __forceinline__ float gelu_t(float x) { const float u = 0.7978845608028654f * (x + 0.044715f * x * x * x); return x * sigm(2.f * u); }
; __device__ __forceinline__ u32x4 pack8(f32x4 v0, f32x4 v1) { u32x4 w; w.x = cvt_pk_bf16(v0[0], v0[1]); w.y = cvt_pk_bf16(v0[2], v0[3]); w.z = cvt_pk_bf16(v1[0], v1[1]); w.w = cvt_pk_bf16(v1[2], v1[3]); return w; }
; template <class T> __device__ __forceinline__ void est(T* p, T v) { if constexpr (MK_EPI_NT != 0) __builtin_nontemporal_store(v, p); else *p = v; }
; __device__ __forceinline__ unsigned pk4_u8(f32x4 v) { return q8(v[0]) | (q8(v[1]) << 8) | (q8(v[2]) << 16) | (q8(v[3]) << 24); }
; __device__ __forceinline__ float sum8sq(f32x4 a, f32x4 b) { return (a[0] * a[0] + a[1] * a[1]) + (a[2] * a[2] + a[3] * a[3]) + (b[0] * b[0] + b[1] * b[1]) + (b[2] * b[2] + b[3] * b[3]); }
; __device__ __forceinline__ float ss_val(const ss_t* ss, int row) { return (float)ss[row] * (1.f / 16777216.f); }
;     __device__ __forceinline__ void operator()(AccT acc, const Unit& u, int wr, int wc, int fr, int fq) const {
;     ...
;             for (int m = 0; m < 4; ++m) { const int row = row0 + ai * 128 + m * 16; const float r = rsqrtf(ss_val(ss, row) * (1.0f / DM) + EPS); bf16_t* rp = O + (size_t)row * NIN + col0; float sq = 0.f;
; #pragma unroll
;                 for (int bj = 0; bj < 2; ++bj) { f32x4 v0 = acc[ai][bj][m][0] * r, v1 = acc[ai][bj][m][1] * r;
;                     if (type == 1 || type == 2) {
; #pragma unroll
;                         for (int j = 0; j < 4; ++j) { v0[j] = gelu_t(v0[j]); v1[j] = gelu_t(v1[j]); }
;                         if (type == 2) sq += sum8sq(v0, v1); }
;                     if (type == 3) {
; #pragma unroll
;                         for (int j = 0; j < 4; ++j) { v0[j] = sigm(v0[j]); v1[j] = sigm(v1[j]); }
;                         est((u32x2*)(G8 + (size_t)row * (NIN - C_G) + (col0 - C_G) + bj * 128), (u32x2)(u32x2){pk4_u8(v0), pk4_u8(v1)}); }
;                     else est((u32x4*)(rp + bj * 128), (u32x4)pack8(v0, v1)); }
;                 if (type == 2) row_atomic(ssv, row, sq, fq); }
.LBB0_509:
	s_waitcnt lgkmcnt(0)
	s_nop 0
	s_and_b64 vcc, exec, s[12:13]
	s_waitcnt vmcnt(0)
	v_mov_b32_e32 v18, v254
	v_mov_b32_e32 v19, v255
	v_ffbh_u32_e32 v20, v19
	v_min_u32_e32 v20, 32, v20
	v_lshlrev_b64 v[18:19], v20, v[18:19]
	v_min_u32_e32 v18, 1, v18
	v_or_b32_e32 v18, v19, v18
	v_cvt_f32_u32_e32 v18, v18
	v_sub_u32_e32 v19, 32, v20
	v_ldexp_f32 v18, v18, v19
	v_mul_f32_e32 v18, 0x33800000, v18
	v_fmamk_f32 v18, v18, 0x3a000000, v164
	v_mul_f32_e32 v19, 0x4b800000, v18
	v_cmp_gt_f32_e64 s[16:17], s89, v18
	s_nop 1
	v_cndmask_b32_e64 v18, v18, v19, s[16:17]
	v_rsq_f32_e32 v18, v18
	s_nop 0
	v_mul_f32_e32 v19, 0x45800000, v18
	v_cndmask_b32_e64 v18, v18, v19, s[16:17]
	v_pk_mul_f32 v[16:17], v[16:17], v[18:19] op_sel_hi:[1,0]
	v_pk_mul_f32 v[24:25], v[14:15], v[18:19] op_sel_hi:[1,0]
	v_pk_mul_f32 v[20:21], v[12:13], v[18:19] op_sel_hi:[1,0]
	v_pk_mul_f32 v[22:23], v[10:11], v[18:19] op_sel_hi:[1,0]
	v_mov_b32_e32 v11, 0
	s_cbranch_vccnz .LBB0_511
	v_mul_f32_e32 v11, 0x3d372713, v22
	v_mul_f32_e32 v11, v22, v11
	v_mul_f32_e32 v12, 0x3d372713, v25
	v_fma_f32 v11, v22, v11, v22
	v_mul_f32_e32 v12, v25, v12
	v_mul_f32_e32 v13, 0x3d372713, v23
	v_mul_f32_e32 v11, 0x3f4c422a, v11
	v_fma_f32 v12, v25, v12, v25
	v_mul_f32_e32 v13, v23, v13
	v_add_f32_e32 v11, v11, v11
	v_mul_f32_e32 v12, 0x3f4c422a, v12
	v_fma_f32 v13, v23, v13, v23
	v_mul_f32_e32 v11, 0xbfb8aa3b, v11
	v_add_f32_e32 v12, v12, v12
	v_mul_f32_e32 v13, 0x3f4c422a, v13
	v_exp_f32_e32 v11, v11
	v_mul_f32_e32 v12, 0xbfb8aa3b, v12
	v_add_f32_e32 v13, v13, v13
	v_exp_f32_e32 v12, v12
	v_mul_f32_e32 v13, 0xbfb8aa3b, v13
	v_exp_f32_e32 v15, v13
	v_add_f32_e32 v11, 1.0, v11
	v_rcp_f32_e32 v13, v11
	v_add_f32_e32 v11, 1.0, v12
	v_rcp_f32_e32 v14, v11
	v_add_f32_e32 v11, 1.0, v15
	v_mul_f32_e32 v12, 0x3d372713, v16
	v_mul_f32_e32 v15, 0x3d372713, v20
	v_mul_f32_e32 v12, v16, v12
	v_mul_f32_e32 v15, v20, v15
	v_fma_f32 v12, v16, v12, v16
	v_fma_f32 v15, v20, v15, v20
	v_mul_f32_e32 v12, 0x3f4c422a, v12
	v_mul_f32_e32 v15, 0x3f4c422a, v15
	v_add_f32_e32 v12, v12, v12
	v_add_f32_e32 v15, v15, v15
	v_mul_f32_e32 v12, 0xbfb8aa3b, v12
	v_mul_f32_e32 v15, 0xbfb8aa3b, v15
	v_exp_f32_e32 v12, v12
	v_exp_f32_e32 v15, v15
	v_rcp_f32_e32 v27, v11
	v_mul_f32_e32 v10, 0x3d372713, v24
	v_add_f32_e32 v11, 1.0, v12
	v_add_f32_e32 v12, 1.0, v15
	v_mul_f32_e32 v15, 0x3d372713, v17
	v_mul_f32_e32 v15, v17, v15
	v_mul_f32_e32 v19, 0x3d372713, v21
	v_mul_f32_e32 v10, v24, v10
	v_fma_f32 v15, v17, v15, v17
	v_mul_f32_e32 v19, v21, v19
	v_fma_f32 v10, v24, v10, v24
	v_mul_f32_e32 v15, 0x3f4c422a, v15
	v_fma_f32 v19, v21, v19, v21
	v_mul_f32_e32 v10, 0x3f4c422a, v10
	v_add_f32_e32 v15, v15, v15
	v_mul_f32_e32 v19, 0x3f4c422a, v19
	v_add_f32_e32 v10, v10, v10
	v_mul_f32_e32 v15, 0xbfb8aa3b, v15
	v_add_f32_e32 v19, v19, v19
	v_mul_f32_e32 v10, 0xbfb8aa3b, v10
	v_exp_f32_e32 v15, v15
	v_mul_f32_e32 v19, 0xbfb8aa3b, v19
	v_exp_f32_e32 v10, v10
	v_exp_f32_e32 v19, v19
	v_add_f32_e32 v15, 1.0, v15
	v_rcp_f32_e32 v15, v15
	v_add_f32_e32 v10, 1.0, v10
	v_add_f32_e32 v19, 1.0, v19
	v_rcp_f32_e32 v10, v10
	v_rcp_f32_e32 v11, v11
	v_rcp_f32_e32 v12, v12
	v_rcp_f32_e32 v26, v19
	v_mov_b32_e32 v29, v16
	v_mov_b32_e32 v16, v25
	v_mov_b32_e32 v28, v24
	v_pk_mul_f32 v[16:17], v[16:17], v[14:15]
	v_mov_b32_e32 v14, v20
	v_mov_b32_e32 v15, v22
	v_mov_b32_e32 v22, v21
	v_pk_mul_f32 v[28:29], v[28:29], v[10:11]
	v_pk_mul_f32 v[10:11], v[16:17], v[16:17]
	v_pk_mul_f32 v[12:13], v[14:15], v[12:13]
	v_pk_mul_f32 v[14:15], v[22:23], v[26:27]
	v_pk_fma_f32 v[10:11], v[28:29], v[28:29], v[10:11]
	v_pk_mul_f32 v[20:21], v[14:15], v[14:15]
	v_add_f32_e32 v10, v10, v11
	v_pk_fma_f32 v[20:21], v[12:13], v[12:13], v[20:21]
	v_mov_b32_e32 v24, v28
	v_add_f32_e32 v10, v21, v10
	v_add_f32_e32 v10, v20, v10
	v_cndmask_b32_e64 v11, 0, v10, s[10:11]
	v_mov_b32_e32 v25, v16
	v_mov_b32_e32 v16, v29
	v_mov_b32_e32 v22, v13
	v_mov_b32_e32 v23, v15
	v_mov_b32_e32 v20, v12
	v_mov_b32_e32 v21, v14

; __device__ __forceinline__ float sigm(float x) { return __builtin_amdgcn_rcpf(1.f + __builtin_amdgcn_exp2f(-1.4426950408889634f * x)); }
; __device__ __forceinline__ float gelu_t(float x) { const float u = 0.7978845608028654f * (x + 0.044715f * x * x * x); return x * sigm(2.f * u); }
; __device__ __forceinline__ u32x4 pack8(f32x4 v0, f32x4 v1) { u32x4 w; w.x = cvt_pk_bf16(v0[0], v0[1]); w.y = cvt_pk_bf16(v0[2], v0[3]); w.z = cvt_pk_bf16(v1[0], v1[1]); w.w = cvt_pk_bf16(v1[2], v1[3]); return w; }
; template <class T> __device__ __forceinline__ void est(T* p, T v) { if constexpr (MK_EPI_NT != 0) __builtin_nontemporal_store(v, p); else *p = v; }
; __device__ __forceinline__ unsigned pk4_u8(f32x4 v) { return q8(v[0]) | (q8(v[1]) << 8) | (q8(v[2]) << 16) | (q8(v[3]) << 24); }
; __device__ __forceinline__ float sum8sq(f32x4 a, f32x4 b) { return (a[0] * a[0] + a[1] * a[1]) + (a[2] * a[2] + a[3] * a[3]) + (b[0] * b[0] + b[1] * b[1]) + (b[2] * b[2] + b[3] * b[3]); }
;     __device__ __forceinline__ void operator()(AccT acc, const Unit& u, int wr, int wc, int fr, int fq) const {
;         const int type = u.pn < 10 ? 0 : (u.pn < 14 ? 1 : (u.pn < 18 ? 2 : 3));
;         const int row0 = u.pm * 256 + wr * 64 + fr, col0 = u.pn * 256 + wc * 32 + 8 * fq;
; #pragma unroll
;         for (int ai = 0; ai < 2; ++ai)
; #pragma unroll
;             for (int m = 0; m < 4; ++m) { const int row = row0 + ai * 128 + m * 16; const float r = rsqrtf(ss_val(ss, row) * (1.0f / DM) + EPS); bf16_t* rp = O + (size_t)row * NIN + col0; float sq = 0.f;
; #pragma unroll
;                 for (int bj = 0; bj < 2; ++bj) { f32x4 v0 = acc[ai][bj][m][0] * r, v1 = acc[ai][bj][m][1] * r;
;                     if (type == 1 || type == 2) {
; #pragma unroll
;                         for (int j = 0; j < 4; ++j) { v0[j] = gelu_t(v0[j]); v1[j] = gelu_t(v1[j]); }
;                         if (type == 2) sq += sum8sq(v0, v1); }
;                     if (type == 3) {
; #pragma unroll
;                         for (int j = 0; j < 4; ++j) { v0[j] = sigm(v0[j]); v1[j] = sigm(v1[j]); }
;                         est((u32x2*)(G8 + (size_t)row * (NIN - C_G) + (col0 - C_G) + bj * 128), (u32x2)(u32x2){pk4_u8(v0), pk4_u8(v1)}); }
;                     else est((u32x4*)(rp + bj * 128), (u32x4)pack8(v0, v1)); }
;                 if (type == 2) row_atomic(ssv, row, sq, fq); }
.LBB0_1361:
	v_lshl_add_u32 v146, s8, 8, v158
	v_ashrrev_i32_e32 v147, 31, v146
	v_lshl_add_u64 v[148:149], v[146:147], 3, s[74:75]
	global_load_dwordx2 v[248:249], v[148:149], off
	global_load_dwordx2 v[250:251], v[148:149], off offset:128
	global_load_dwordx2 v[252:253], v[148:149], off offset:256
	global_load_dwordx2 v[254:255], v[148:149], off offset:384
	s_cmp_lt_u32 s16, 18
	s_cselect_b32 s9, 2, 3
	s_cmp_gt_u32 s16, 13
	s_cselect_b32 s9, s9, 1
	s_cmp_gt_i32 s16, 9
	s_cselect_b32 s12, s9, 0
	s_cmp_eq_u32 s12, 2
	s_cselect_b64 s[10:11], -1, 0
	s_add_i32 s13, s12, -1
	s_cmp_lt_u32 s13, 2
	s_cselect_b64 s[8:9], -1, 0
	s_cmp_gt_u32 s13, 1
	v_mov_b32_e32 v167, 0
	s_waitcnt vmcnt(3)
	v_mov_b32_e32 v150, v248
	v_mov_b32_e32 v151, v249
	global_load_dwordx2 v[248:249], v[148:149], off offset:1024
	v_ffbh_u32_e32 v152, v151
	v_min_u32_e32 v152, 32, v152
	v_lshlrev_b64 v[150:151], v152, v[150:151]
	v_min_u32_e32 v150, 1, v150
	v_or_b32_e32 v150, v151, v150
	v_cvt_f32_u32_e32 v150, v150
	v_sub_u32_e32 v151, 32, v152
	v_ldexp_f32 v150, v150, v151
	v_mul_f32_e32 v150, 0x33800000, v150
	v_fmamk_f32 v150, v150, 0x3a000000, v164
	v_cmp_gt_f32_e32 vcc, s95, v150
	v_mul_f32_e32 v151, 0x4b800000, v150
	s_nop 0
	v_cndmask_b32_e32 v150, v150, v151, vcc
	v_rsq_f32_e32 v150, v150
	s_nop 0
	v_mul_f32_e32 v151, 0x45800000, v150
	v_cndmask_b32_e32 v150, v150, v151, vcc
	v_pk_mul_f32 v[128:129], v[128:129], v[150:151] op_sel_hi:[1,0]
	v_pk_mul_f32 v[156:157], v[126:127], v[150:151] op_sel_hi:[1,0]
	v_pk_mul_f32 v[152:153], v[124:125], v[150:151] op_sel_hi:[1,0]
	v_pk_mul_f32 v[154:155], v[122:123], v[150:151] op_sel_hi:[1,0]
	s_cbranch_scc1 .LBB0_1363
	v_mul_f32_e32 v123, 0x3d372713, v154
	v_mul_f32_e32 v123, v154, v123
	v_mul_f32_e32 v124, 0x3d372713, v157
	v_fma_f32 v123, v154, v123, v154
	v_mul_f32_e32 v124, v157, v124
	v_mul_f32_e32 v125, 0x3d372713, v155
	v_mul_f32_e32 v123, 0x3f4c422a, v123
	v_fma_f32 v124, v157, v124, v157
	v_mul_f32_e32 v125, v155, v125
	v_add_f32_e32 v123, v123, v123
	v_mul_f32_e32 v124, 0x3f4c422a, v124
	v_fma_f32 v125, v155, v125, v155
	v_mul_f32_e32 v123, 0xbfb8aa3b, v123
	v_add_f32_e32 v124, v124, v124
	v_mul_f32_e32 v125, 0x3f4c422a, v125
	v_exp_f32_e32 v123, v123
	v_mul_f32_e32 v124, 0xbfb8aa3b, v124
	v_add_f32_e32 v125, v125, v125
	v_exp_f32_e32 v124, v124
	v_mul_f32_e32 v125, 0xbfb8aa3b, v125
	v_exp_f32_e32 v127, v125
	v_add_f32_e32 v123, 1.0, v123
	v_rcp_f32_e32 v125, v123
	v_add_f32_e32 v123, 1.0, v124
	v_rcp_f32_e32 v126, v123
	v_add_f32_e32 v123, 1.0, v127
	v_mul_f32_e32 v124, 0x3d372713, v128
	v_mul_f32_e32 v127, 0x3d372713, v152
	v_mul_f32_e32 v124, v128, v124
	v_mul_f32_e32 v127, v152, v127
	v_fma_f32 v124, v128, v124, v128
	v_fma_f32 v127, v152, v127, v152
	v_mul_f32_e32 v124, 0x3f4c422a, v124
	v_mul_f32_e32 v127, 0x3f4c422a, v127
	v_add_f32_e32 v124, v124, v124
	v_add_f32_e32 v127, v127, v127
	v_mul_f32_e32 v124, 0xbfb8aa3b, v124
	v_mul_f32_e32 v127, 0xbfb8aa3b, v127
	v_exp_f32_e32 v124, v124
	v_exp_f32_e32 v127, v127
	v_rcp_f32_e32 v169, v123
	v_mul_f32_e32 v122, 0x3d372713, v156
	v_add_f32_e32 v123, 1.0, v124
	v_add_f32_e32 v124, 1.0, v127
	v_mul_f32_e32 v127, 0x3d372713, v129
	v_mul_f32_e32 v127, v129, v127
	v_mul_f32_e32 v151, 0x3d372713, v153
	v_mul_f32_e32 v122, v156, v122
	v_fma_f32 v127, v129, v127, v129
	v_mul_f32_e32 v151, v153, v151
	v_fma_f32 v122, v156, v122, v156
	v_mul_f32_e32 v127, 0x3f4c422a, v127
	v_fma_f32 v151, v153, v151, v153
	v_mul_f32_e32 v122, 0x3f4c422a, v122
	v_add_f32_e32 v127, v127, v127
	v_mul_f32_e32 v151, 0x3f4c422a, v151
	v_add_f32_e32 v122, v122, v122
	v_mul_f32_e32 v127, 0xbfb8aa3b, v127
	v_add_f32_e32 v151, v151, v151
	v_mul_f32_e32 v122, 0xbfb8aa3b, v122
	v_exp_f32_e32 v127, v127
	v_mul_f32_e32 v151, 0xbfb8aa3b, v151
	v_exp_f32_e32 v122, v122
	v_exp_f32_e32 v151, v151
	v_add_f32_e32 v127, 1.0, v127
	v_rcp_f32_e32 v127, v127
	v_add_f32_e32 v122, 1.0, v122
	v_add_f32_e32 v151, 1.0, v151
	v_rcp_f32_e32 v122, v122
	v_rcp_f32_e32 v123, v123
	v_rcp_f32_e32 v168, v151
	v_rcp_f32_e32 v124, v124
	v_mov_b32_e32 v171, v128
	v_mov_b32_e32 v128, v157
	v_mov_b32_e32 v170, v156
	v_pk_mul_f32 v[128:129], v[128:129], v[126:127]
	v_mov_b32_e32 v157, v154
	v_mov_b32_e32 v154, v153
	v_pk_mul_f32 v[122:123], v[170:171], v[122:123]
	v_pk_mul_f32 v[126:127], v[128:129], v[128:129]
	v_mov_b32_e32 v156, v152
	v_pk_mul_f32 v[168:169], v[154:155], v[168:169]
	v_pk_fma_f32 v[126:127], v[122:123], v[122:123], v[126:127]
	v_pk_mul_f32 v[124:125], v[156:157], v[124:125]
	v_pk_mul_f32 v[152:153], v[168:169], v[168:169]
	v_add_f32_e32 v126, v126, v127
	v_pk_fma_f32 v[152:153], v[124:125], v[124:125], v[152:153]
	v_mov_b32_e32 v156, v122
	v_add_f32_e32 v126, v153, v126
	v_add_f32_e32 v126, v152, v126
	v_cndmask_b32_e64 v167, 0, v126, s[10:11]
	v_mov_b32_e32 v157, v128
	v_mov_b32_e32 v128, v123
	v_mov_b32_e32 v154, v125
	v_mov_b32_e32 v155, v169
	v_mov_b32_e32 v152, v124
	v_mov_b32_e32 v153, v168

; __device__ __forceinline__ float sigm(float x) { return __builtin_amdgcn_rcpf(1.f + __builtin_amdgcn_exp2f(-1.4426950408889634f * x)); }
; __device__ __forceinline__ float gelu_t(float x) { const float u = 0.7978845608028654f * (x + 0.044715f * x * x * x); return x * sigm(2.f * u); }
; __device__ __forceinline__ u32x4 pack8(f32x4 v0, f32x4 v1) { u32x4 w; w.x = cvt_pk_bf16(v0[0], v0[1]); w.y = cvt_pk_bf16(v0[2], v0[3]); w.z = cvt_pk_bf16(v1[0], v1[1]); w.w = cvt_pk_bf16(v1[2], v1[3]); return w; }
; template <class T> __device__ __forceinline__ void est(T* p, T v) { if constexpr (MK_EPI_NT != 0) __builtin_nontemporal_store(v, p); else *p = v; }
; __device__ __forceinline__ unsigned pk4_u8(f32x4 v) { return q8(v[0]) | (q8(v[1]) << 8) | (q8(v[2]) << 16) | (q8(v[3]) << 24); }
; __device__ __forceinline__ float sum8sq(f32x4 a, f32x4 b) { return (a[0] * a[0] + a[1] * a[1]) + (a[2] * a[2] + a[3] * a[3]) + (b[0] * b[0] + b[1] * b[1]) + (b[2] * b[2] + b[3] * b[3]); }
; __device__ __forceinline__ float ss_val(const ss_t* ss, int row) { return (float)ss[row] * (1.f / 16777216.f); }
;     __device__ __forceinline__ void operator()(AccT acc, const Unit& u, int wr, int wc, int fr, int fq) const {
;     ...
;             for (int m = 0; m < 4; ++m) { const int row = row0 + ai * 128 + m * 16; const float r = rsqrtf(ss_val(ss, row) * (1.0f / DM) + EPS); bf16_t* rp = O + (size_t)row * NIN + col0; float sq = 0.f;
; #pragma unroll
;                 for (int bj = 0; bj < 2; ++bj) { f32x4 v0 = acc[ai][bj][m][0] * r, v1 = acc[ai][bj][m][1] * r;
;                     if (type == 1 || type == 2) {
; #pragma unroll
;                         for (int j = 0; j < 4; ++j) { v0[j] = gelu_t(v0[j]); v1[j] = gelu_t(v1[j]); }
;                         if (type == 2) sq += sum8sq(v0, v1); }
;                     if (type == 3) {
; #pragma unroll
;                         for (int j = 0; j < 4; ++j) { v0[j] = sigm(v0[j]); v1[j] = sigm(v1[j]); }
;                         est((u32x2*)(G8 + (size_t)row * (NIN - C_G) + (col0 - C_G) + bj * 128), (u32x2)(u32x2){pk4_u8(v0), pk4_u8(v1)}); }
;                     else est((u32x4*)(rp + bj * 128), (u32x4)pack8(v0, v1)); }
;                 if (type == 2) row_atomic(ssv, row, sq, fq); }
.LBB0_1379:
	v_or_b32_e32 v114, 16, v146
	s_waitcnt lgkmcnt(0)
	v_ashrrev_i32_e32 v115, 31, v114
	v_lshl_add_u64 v[116:117], v[114:115], 3, s[74:75]
	s_nop 0
	s_and_b64 vcc, exec, s[12:13]
	v_mov_b32_e32 v124, 0
	s_waitcnt vmcnt(3)
	v_mov_b32_e32 v116, v250
	v_mov_b32_e32 v117, v251
	global_load_dwordx2 v[250:251], v[148:149], off offset:1152
	v_ffbh_u32_e32 v118, v117
	v_min_u32_e32 v118, 32, v118
	v_lshlrev_b64 v[116:117], v118, v[116:117]
	v_min_u32_e32 v116, 1, v116
	v_or_b32_e32 v116, v117, v116
	v_cvt_f32_u32_e32 v116, v116
	v_sub_u32_e32 v117, 32, v118
	v_ldexp_f32 v116, v116, v117
	v_mul_f32_e32 v116, 0x33800000, v116
	v_fmamk_f32 v116, v116, 0x3a000000, v164
	v_mul_f32_e32 v117, 0x4b800000, v116
	v_cmp_gt_f32_e64 s[16:17], s95, v116
	s_nop 1
	v_cndmask_b32_e64 v116, v116, v117, s[16:17]
	v_rsq_f32_e32 v116, v116
	s_nop 0
	v_mul_f32_e32 v117, 0x45800000, v116
	v_cndmask_b32_e64 v116, v116, v117, s[16:17]
	v_pk_mul_f32 v[112:113], v[112:113], v[116:117] op_sel_hi:[1,0]
	v_pk_mul_f32 v[120:121], v[110:111], v[116:117] op_sel_hi:[1,0]
	v_pk_mul_f32 v[110:111], v[108:109], v[116:117] op_sel_hi:[1,0]
	v_pk_mul_f32 v[118:119], v[106:107], v[116:117] op_sel_hi:[1,0]
	s_cbranch_vccnz .LBB0_1381
	v_mul_f32_e32 v107, 0x3d372713, v118
	v_mul_f32_e32 v107, v118, v107
	v_mul_f32_e32 v108, 0x3d372713, v121
	v_fma_f32 v107, v118, v107, v118
	v_mul_f32_e32 v108, v121, v108
	v_mul_f32_e32 v109, 0x3d372713, v119
	v_mul_f32_e32 v107, 0x3f4c422a, v107
	v_fma_f32 v108, v121, v108, v121
	v_mul_f32_e32 v109, v119, v109
	v_add_f32_e32 v107, v107, v107
	v_mul_f32_e32 v108, 0x3f4c422a, v108
	v_fma_f32 v109, v119, v109, v119
	v_mul_f32_e32 v107, 0xbfb8aa3b, v107
	v_add_f32_e32 v108, v108, v108
	v_mul_f32_e32 v109, 0x3f4c422a, v109
	v_exp_f32_e32 v107, v107
	v_mul_f32_e32 v108, 0xbfb8aa3b, v108
	v_add_f32_e32 v109, v109, v109
	v_exp_f32_e32 v108, v108
	v_mul_f32_e32 v109, 0xbfb8aa3b, v109
	v_exp_f32_e32 v117, v109
	v_add_f32_e32 v107, 1.0, v107
	v_rcp_f32_e32 v109, v107
	v_add_f32_e32 v107, 1.0, v108
	v_rcp_f32_e32 v124, v107
	v_add_f32_e32 v107, 1.0, v117
	v_mul_f32_e32 v108, 0x3d372713, v112
	v_mul_f32_e32 v117, 0x3d372713, v110
	v_mul_f32_e32 v108, v112, v108
	v_mul_f32_e32 v117, v110, v117
	v_fma_f32 v108, v112, v108, v112
	v_fma_f32 v117, v110, v117, v110
	v_mul_f32_e32 v108, 0x3f4c422a, v108
	v_mul_f32_e32 v117, 0x3f4c422a, v117
	v_add_f32_e32 v108, v108, v108
	v_add_f32_e32 v117, v117, v117
	v_mul_f32_e32 v108, 0xbfb8aa3b, v108
	v_mul_f32_e32 v117, 0xbfb8aa3b, v117
	v_exp_f32_e32 v108, v108
	v_exp_f32_e32 v117, v117
	v_rcp_f32_e32 v127, v107
	v_mul_f32_e32 v106, 0x3d372713, v120
	v_add_f32_e32 v107, 1.0, v108
	v_add_f32_e32 v108, 1.0, v117
	v_mul_f32_e32 v117, 0x3d372713, v113
	v_mul_f32_e32 v117, v113, v117
	v_mul_f32_e32 v125, 0x3d372713, v111
	v_mul_f32_e32 v106, v120, v106
	v_fma_f32 v117, v113, v117, v113
	v_mul_f32_e32 v125, v111, v125
	v_fma_f32 v106, v120, v106, v120
	v_mul_f32_e32 v117, 0x3f4c422a, v117
	v_fma_f32 v125, v111, v125, v111
	v_mul_f32_e32 v106, 0x3f4c422a, v106
	v_add_f32_e32 v117, v117, v117
	v_mul_f32_e32 v125, 0x3f4c422a, v125
	v_add_f32_e32 v106, v106, v106
	v_mul_f32_e32 v117, 0xbfb8aa3b, v117
	v_add_f32_e32 v125, v125, v125
	v_mul_f32_e32 v106, 0xbfb8aa3b, v106
	v_exp_f32_e32 v117, v117
	v_mul_f32_e32 v125, 0xbfb8aa3b, v125
	v_exp_f32_e32 v106, v106
	v_exp_f32_e32 v126, v125
	v_add_f32_e32 v117, 1.0, v117
	v_rcp_f32_e32 v125, v117
	v_add_f32_e32 v106, 1.0, v106
	v_add_f32_e32 v117, 1.0, v126
	v_rcp_f32_e32 v106, v106
	v_rcp_f32_e32 v107, v107
	v_rcp_f32_e32 v126, v117
	v_rcp_f32_e32 v108, v108
	v_mov_b32_e32 v129, v112
	v_mov_b32_e32 v112, v121
	v_mov_b32_e32 v128, v120
	v_pk_mul_f32 v[112:113], v[112:113], v[124:125]
	v_mov_b32_e32 v125, v118
	v_mov_b32_e32 v118, v111
	v_pk_mul_f32 v[106:107], v[128:129], v[106:107]
	v_pk_mul_f32 v[120:121], v[112:113], v[112:113]
	v_mov_b32_e32 v124, v110
	v_pk_mul_f32 v[126:127], v[118:119], v[126:127]
	v_pk_fma_f32 v[120:121], v[106:107], v[106:107], v[120:121]
	v_pk_mul_f32 v[108:109], v[124:125], v[108:109]
	v_pk_mul_f32 v[110:111], v[126:127], v[126:127]
	v_add_f32_e32 v117, v120, v121
	v_pk_fma_f32 v[110:111], v[108:109], v[108:109], v[110:111]
	v_mov_b32_e32 v120, v106
	v_add_f32_e32 v111, v111, v117
	v_add_f32_e32 v110, v110, v111
	v_cndmask_b32_e64 v124, 0, v110, s[10:11]
	v_mov_b32_e32 v121, v112
	v_mov_b32_e32 v112, v107
	v_mov_b32_e32 v118, v109
	v_mov_b32_e32 v119, v127
	v_mov_b32_e32 v110, v108
	v_mov_b32_e32 v111, v126

; __device__ __forceinline__ float sigm(float x) { return __builtin_amdgcn_rcpf(1.f + __builtin_amdgcn_exp2f(-1.4426950408889634f * x)); }
; __device__ __forceinline__ float gelu_t(float x) { const float u = 0.7978845608028654f * (x + 0.044715f * x * x * x); return x * sigm(2.f * u); }
; __device__ __forceinline__ u32x4 pack8(f32x4 v0, f32x4 v1) { u32x4 w; w.x = cvt_pk_bf16(v0[0], v0[1]); w.y = cvt_pk_bf16(v0[2], v0[3]); w.z = cvt_pk_bf16(v1[0], v1[1]); w.w = cvt_pk_bf16(v1[2], v1[3]); return w; }
; template <class T> __device__ __forceinline__ void est(T* p, T v) { if constexpr (MK_EPI_NT != 0) __builtin_nontemporal_store(v, p); else *p = v; }
; __device__ __forceinline__ unsigned pk4_u8(f32x4 v) { return q8(v[0]) | (q8(v[1]) << 8) | (q8(v[2]) << 16) | (q8(v[3]) << 24); }
; __device__ __forceinline__ float sum8sq(f32x4 a, f32x4 b) { return (a[0] * a[0] + a[1] * a[1]) + (a[2] * a[2] + a[3] * a[3]) + (b[0] * b[0] + b[1] * b[1]) + (b[2] * b[2] + b[3] * b[3]); }
; __device__ __forceinline__ float ss_val(const ss_t* ss, int row) { return (float)ss[row] * (1.f / 16777216.f); }
;     __device__ __forceinline__ void operator()(AccT acc, const Unit& u, int wr, int wc, int fr, int fq) const {
;     ...
;             for (int m = 0; m < 4; ++m) { const int row = row0 + ai * 128 + m * 16; const float r = rsqrtf(ss_val(ss, row) * (1.0f / DM) + EPS); bf16_t* rp = O + (size_t)row * NIN + col0; float sq = 0.f;
; #pragma unroll
;                 for (int bj = 0; bj < 2; ++bj) { f32x4 v0 = acc[ai][bj][m][0] * r, v1 = acc[ai][bj][m][1] * r;
;                     if (type == 1 || type == 2) {
; #pragma unroll
;                         for (int j = 0; j < 4; ++j) { v0[j] = gelu_t(v0[j]); v1[j] = gelu_t(v1[j]); }
;                         if (type == 2) sq += sum8sq(v0, v1); }
;                     if (type == 3) {
; #pragma unroll
;                         for (int j = 0; j < 4; ++j) { v0[j] = sigm(v0[j]); v1[j] = sigm(v1[j]); }
;                         est((u32x2*)(G8 + (size_t)row * (NIN - C_G) + (col0 - C_G) + bj * 128), (u32x2)(u32x2){pk4_u8(v0), pk4_u8(v1)}); }
;                     else est((u32x4*)(rp + bj * 128), (u32x4)pack8(v0, v1)); }
;                 if (type == 2) row_atomic(ssv, row, sq, fq); }
.LBB0_1397:
	v_or_b32_e32 v98, 32, v146
	s_waitcnt lgkmcnt(0)
	v_ashrrev_i32_e32 v99, 31, v98
	v_lshl_add_u64 v[100:101], v[98:99], 3, s[74:75]
	s_nop 0
	s_and_b64 vcc, exec, s[12:13]
	v_mov_b32_e32 v106, 0
	s_waitcnt vmcnt(3)
	v_mov_b32_e32 v100, v252
	v_mov_b32_e32 v101, v253
	global_load_dwordx2 v[252:253], v[148:149], off offset:1280
	v_ffbh_u32_e32 v102, v101
	v_min_u32_e32 v102, 32, v102
	v_lshlrev_b64 v[100:101], v102, v[100:101]
	v_min_u32_e32 v100, 1, v100
	v_or_b32_e32 v100, v101, v100
	v_cvt_f32_u32_e32 v100, v100
	v_sub_u32_e32 v101, 32, v102
	v_ldexp_f32 v100, v100, v101
	v_mul_f32_e32 v100, 0x33800000, v100
	v_fmamk_f32 v100, v100, 0x3a000000, v164
	v_mul_f32_e32 v101, 0x4b800000, v100
	v_cmp_gt_f32_e64 s[16:17], s95, v100
	s_nop 1
	v_cndmask_b32_e64 v100, v100, v101, s[16:17]
	v_rsq_f32_e32 v100, v100
	s_nop 0
	v_mul_f32_e32 v101, 0x45800000, v100
	v_cndmask_b32_e64 v100, v100, v101, s[16:17]
	v_pk_mul_f32 v[96:97], v[96:97], v[100:101] op_sel_hi:[1,0]
	v_pk_mul_f32 v[104:105], v[94:95], v[100:101] op_sel_hi:[1,0]
	v_pk_mul_f32 v[94:95], v[92:93], v[100:101] op_sel_hi:[1,0]
	v_pk_mul_f32 v[102:103], v[90:91], v[100:101] op_sel_hi:[1,0]
	s_cbranch_vccnz .LBB0_1399
	v_mul_f32_e32 v91, 0x3d372713, v102
	v_mul_f32_e32 v91, v102, v91
	v_mul_f32_e32 v92, 0x3d372713, v105
	v_fma_f32 v91, v102, v91, v102
	v_mul_f32_e32 v92, v105, v92
	v_mul_f32_e32 v93, 0x3d372713, v103
	v_mul_f32_e32 v91, 0x3f4c422a, v91
	v_fma_f32 v92, v105, v92, v105
	v_mul_f32_e32 v93, v103, v93
	v_add_f32_e32 v91, v91, v91
	v_mul_f32_e32 v92, 0x3f4c422a, v92
	v_fma_f32 v93, v103, v93, v103
	v_mul_f32_e32 v91, 0xbfb8aa3b, v91
	v_add_f32_e32 v92, v92, v92
	v_mul_f32_e32 v93, 0x3f4c422a, v93
	v_exp_f32_e32 v91, v91
	v_mul_f32_e32 v92, 0xbfb8aa3b, v92
	v_add_f32_e32 v93, v93, v93
	v_exp_f32_e32 v92, v92
	v_mul_f32_e32 v93, 0xbfb8aa3b, v93
	v_exp_f32_e32 v101, v93
	v_add_f32_e32 v91, 1.0, v91
	v_rcp_f32_e32 v93, v91
	v_add_f32_e32 v91, 1.0, v92
	v_rcp_f32_e32 v106, v91
	v_add_f32_e32 v91, 1.0, v101
	v_mul_f32_e32 v92, 0x3d372713, v96
	v_mul_f32_e32 v101, 0x3d372713, v94
	v_mul_f32_e32 v92, v96, v92
	v_mul_f32_e32 v101, v94, v101
	v_fma_f32 v92, v96, v92, v96
	v_fma_f32 v101, v94, v101, v94
	v_mul_f32_e32 v92, 0x3f4c422a, v92
	v_mul_f32_e32 v101, 0x3f4c422a, v101
	v_add_f32_e32 v92, v92, v92
	v_add_f32_e32 v101, v101, v101
	v_mul_f32_e32 v92, 0xbfb8aa3b, v92
	v_mul_f32_e32 v101, 0xbfb8aa3b, v101
	v_exp_f32_e32 v92, v92
	v_exp_f32_e32 v101, v101
	v_rcp_f32_e32 v109, v91
	v_mul_f32_e32 v90, 0x3d372713, v104
	v_add_f32_e32 v91, 1.0, v92
	v_add_f32_e32 v92, 1.0, v101
	v_mul_f32_e32 v101, 0x3d372713, v97
	v_mul_f32_e32 v101, v97, v101
	v_mul_f32_e32 v107, 0x3d372713, v95
	v_mul_f32_e32 v90, v104, v90
	v_fma_f32 v101, v97, v101, v97
	v_mul_f32_e32 v107, v95, v107
	v_fma_f32 v90, v104, v90, v104
	v_mul_f32_e32 v101, 0x3f4c422a, v101
	v_fma_f32 v107, v95, v107, v95
	v_mul_f32_e32 v90, 0x3f4c422a, v90
	v_add_f32_e32 v101, v101, v101
	v_mul_f32_e32 v107, 0x3f4c422a, v107
	v_add_f32_e32 v90, v90, v90
	v_mul_f32_e32 v101, 0xbfb8aa3b, v101
	v_add_f32_e32 v107, v107, v107
	v_mul_f32_e32 v90, 0xbfb8aa3b, v90
	v_exp_f32_e32 v101, v101
	v_mul_f32_e32 v107, 0xbfb8aa3b, v107
	v_exp_f32_e32 v90, v90
	v_exp_f32_e32 v108, v107
	v_add_f32_e32 v101, 1.0, v101
	v_rcp_f32_e32 v107, v101
	v_add_f32_e32 v90, 1.0, v90
	v_add_f32_e32 v101, 1.0, v108
	v_rcp_f32_e32 v90, v90
	v_rcp_f32_e32 v91, v91
	v_rcp_f32_e32 v108, v101
	v_rcp_f32_e32 v92, v92
	v_mov_b32_e32 v111, v96
	v_mov_b32_e32 v96, v105
	v_mov_b32_e32 v110, v104
	v_pk_mul_f32 v[96:97], v[96:97], v[106:107]
	v_mov_b32_e32 v107, v102
	v_mov_b32_e32 v102, v95
	v_pk_mul_f32 v[90:91], v[110:111], v[90:91]
	v_pk_mul_f32 v[104:105], v[96:97], v[96:97]
	v_mov_b32_e32 v106, v94
	v_pk_mul_f32 v[108:109], v[102:103], v[108:109]
	v_pk_fma_f32 v[104:105], v[90:91], v[90:91], v[104:105]
	v_pk_mul_f32 v[92:93], v[106:107], v[92:93]
	v_pk_mul_f32 v[94:95], v[108:109], v[108:109]
	v_add_f32_e32 v101, v104, v105
	v_pk_fma_f32 v[94:95], v[92:93], v[92:93], v[94:95]
	v_mov_b32_e32 v104, v90
	v_add_f32_e32 v95, v95, v101
	v_add_f32_e32 v94, v94, v95
	v_cndmask_b32_e64 v106, 0, v94, s[10:11]
	v_mov_b32_e32 v105, v96
	v_mov_b32_e32 v96, v91
	v_mov_b32_e32 v102, v93
	v_mov_b32_e32 v103, v109
	v_mov_b32_e32 v94, v92
	v_mov_b32_e32 v95, v108

; __device__ __forceinline__ float sigm(float x) { return __builtin_amdgcn_rcpf(1.f + __builtin_amdgcn_exp2f(-1.4426950408889634f * x)); }
; __device__ __forceinline__ float gelu_t(float x) { const float u = 0.7978845608028654f * (x + 0.044715f * x * x * x); return x * sigm(2.f * u); }
; __device__ __forceinline__ u32x4 pack8(f32x4 v0, f32x4 v1) { u32x4 w; w.x = cvt_pk_bf16(v0[0], v0[1]); w.y = cvt_pk_bf16(v0[2], v0[3]); w.z = cvt_pk_bf16(v1[0], v1[1]); w.w = cvt_pk_bf16(v1[2], v1[3]); return w; }
; template <class T> __device__ __forceinline__ void est(T* p, T v) { if constexpr (MK_EPI_NT != 0) __builtin_nontemporal_store(v, p); else *p = v; }
; __device__ __forceinline__ unsigned pk4_u8(f32x4 v) { return q8(v[0]) | (q8(v[1]) << 8) | (q8(v[2]) << 16) | (q8(v[3]) << 24); }
; __device__ __forceinline__ float sum8sq(f32x4 a, f32x4 b) { return (a[0] * a[0] + a[1] * a[1]) + (a[2] * a[2] + a[3] * a[3]) + (b[0] * b[0] + b[1] * b[1]) + (b[2] * b[2] + b[3] * b[3]); }
; __device__ __forceinline__ float ss_val(const ss_t* ss, int row) { return (float)ss[row] * (1.f / 16777216.f); }
;     __device__ __forceinline__ void operator()(AccT acc, const Unit& u, int wr, int wc, int fr, int fq) const {
;     ...
;             for (int m = 0; m < 4; ++m) { const int row = row0 + ai * 128 + m * 16; const float r = rsqrtf(ss_val(ss, row) * (1.0f / DM) + EPS); bf16_t* rp = O + (size_t)row * NIN + col0; float sq = 0.f;
; #pragma unroll
;                 for (int bj = 0; bj < 2; ++bj) { f32x4 v0 = acc[ai][bj][m][0] * r, v1 = acc[ai][bj][m][1] * r;
;                     if (type == 1 || type == 2) {
; #pragma unroll
;                         for (int j = 0; j < 4; ++j) { v0[j] = gelu_t(v0[j]); v1[j] = gelu_t(v1[j]); }
;                         if (type == 2) sq += sum8sq(v0, v1); }
;                     if (type == 3) {
; #pragma unroll
;                         for (int j = 0; j < 4; ++j) { v0[j] = sigm(v0[j]); v1[j] = sigm(v1[j]); }
;                         est((u32x2*)(G8 + (size_t)row * (NIN - C_G) + (col0 - C_G) + bj * 128), (u32x2)(u32x2){pk4_u8(v0), pk4_u8(v1)}); }
;                     else est((u32x4*)(rp + bj * 128), (u32x4)pack8(v0, v1)); }
;                 if (type == 2) row_atomic(ssv, row, sq, fq); }
.LBB0_1415:
	v_or_b32_e32 v82, 48, v146
	s_waitcnt lgkmcnt(0)
	v_ashrrev_i32_e32 v83, 31, v82
	v_lshl_add_u64 v[84:85], v[82:83], 3, s[74:75]
	s_nop 0
	s_and_b64 vcc, exec, s[12:13]
	v_mov_b32_e32 v90, 0
	s_waitcnt vmcnt(3)
	v_mov_b32_e32 v84, v254
	v_mov_b32_e32 v85, v255
	global_load_dwordx2 v[254:255], v[148:149], off offset:1408
	v_ffbh_u32_e32 v86, v85
	v_min_u32_e32 v86, 32, v86
	v_lshlrev_b64 v[84:85], v86, v[84:85]
	v_min_u32_e32 v84, 1, v84
	v_or_b32_e32 v84, v85, v84
	v_cvt_f32_u32_e32 v84, v84
	v_sub_u32_e32 v85, 32, v86
	v_ldexp_f32 v84, v84, v85
	v_mul_f32_e32 v84, 0x33800000, v84
	v_fmamk_f32 v84, v84, 0x3a000000, v164
	v_mul_f32_e32 v85, 0x4b800000, v84
	v_cmp_gt_f32_e64 s[16:17], s95, v84
	s_nop 1
	v_cndmask_b32_e64 v84, v84, v85, s[16:17]
	v_rsq_f32_e32 v84, v84
	s_nop 0
	v_mul_f32_e32 v85, 0x45800000, v84
	v_cndmask_b32_e64 v84, v84, v85, s[16:17]
	v_pk_mul_f32 v[80:81], v[80:81], v[84:85] op_sel_hi:[1,0]
	v_pk_mul_f32 v[88:89], v[78:79], v[84:85] op_sel_hi:[1,0]
	v_pk_mul_f32 v[78:79], v[76:77], v[84:85] op_sel_hi:[1,0]
	v_pk_mul_f32 v[86:87], v[74:75], v[84:85] op_sel_hi:[1,0]
	s_cbranch_vccnz .LBB0_1417
	v_mul_f32_e32 v75, 0x3d372713, v86
	v_mul_f32_e32 v75, v86, v75
	v_mul_f32_e32 v76, 0x3d372713, v89
	v_fma_f32 v75, v86, v75, v86
	v_mul_f32_e32 v76, v89, v76
	v_mul_f32_e32 v77, 0x3d372713, v87
	v_mul_f32_e32 v75, 0x3f4c422a, v75
	v_fma_f32 v76, v89, v76, v89
	v_mul_f32_e32 v77, v87, v77
	v_add_f32_e32 v75, v75, v75
	v_mul_f32_e32 v76, 0x3f4c422a, v76
	v_fma_f32 v77, v87, v77, v87
	v_mul_f32_e32 v75, 0xbfb8aa3b, v75
	v_add_f32_e32 v76, v76, v76
	v_mul_f32_e32 v77, 0x3f4c422a, v77
	v_exp_f32_e32 v75, v75
	v_mul_f32_e32 v76, 0xbfb8aa3b, v76
	v_add_f32_e32 v77, v77, v77
	v_exp_f32_e32 v76, v76
	v_mul_f32_e32 v77, 0xbfb8aa3b, v77
	v_exp_f32_e32 v85, v77
	v_add_f32_e32 v75, 1.0, v75
	v_rcp_f32_e32 v77, v75
	v_add_f32_e32 v75, 1.0, v76
	v_rcp_f32_e32 v90, v75
	v_add_f32_e32 v75, 1.0, v85
	v_mul_f32_e32 v76, 0x3d372713, v80
	v_mul_f32_e32 v85, 0x3d372713, v78
	v_mul_f32_e32 v76, v80, v76
	v_mul_f32_e32 v85, v78, v85
	v_fma_f32 v76, v80, v76, v80
	v_fma_f32 v85, v78, v85, v78
	v_mul_f32_e32 v76, 0x3f4c422a, v76
	v_mul_f32_e32 v85, 0x3f4c422a, v85
	v_add_f32_e32 v76, v76, v76
	v_add_f32_e32 v85, v85, v85
	v_mul_f32_e32 v76, 0xbfb8aa3b, v76
	v_mul_f32_e32 v85, 0xbfb8aa3b, v85
	v_exp_f32_e32 v76, v76
	v_exp_f32_e32 v85, v85
	v_rcp_f32_e32 v93, v75
	v_mul_f32_e32 v74, 0x3d372713, v88
	v_add_f32_e32 v75, 1.0, v76
	v_add_f32_e32 v76, 1.0, v85
	v_mul_f32_e32 v85, 0x3d372713, v81
	v_mul_f32_e32 v85, v81, v85
	v_mul_f32_e32 v91, 0x3d372713, v79
	v_mul_f32_e32 v74, v88, v74
	v_fma_f32 v85, v81, v85, v81
	v_mul_f32_e32 v91, v79, v91
	v_fma_f32 v74, v88, v74, v88
	v_mul_f32_e32 v85, 0x3f4c422a, v85
	v_fma_f32 v91, v79, v91, v79
	v_mul_f32_e32 v74, 0x3f4c422a, v74
	v_add_f32_e32 v85, v85, v85
	v_mul_f32_e32 v91, 0x3f4c422a, v91
	v_add_f32_e32 v74, v74, v74
	v_mul_f32_e32 v85, 0xbfb8aa3b, v85
	v_add_f32_e32 v91, v91, v91
	v_mul_f32_e32 v74, 0xbfb8aa3b, v74
	v_exp_f32_e32 v85, v85
	v_mul_f32_e32 v91, 0xbfb8aa3b, v91
	v_exp_f32_e32 v74, v74
	v_exp_f32_e32 v92, v91
	v_add_f32_e32 v85, 1.0, v85
	v_rcp_f32_e32 v91, v85
	v_add_f32_e32 v74, 1.0, v74
	v_add_f32_e32 v85, 1.0, v92
	v_rcp_f32_e32 v74, v74
	v_rcp_f32_e32 v75, v75
	v_rcp_f32_e32 v92, v85
	v_rcp_f32_e32 v76, v76
	v_mov_b32_e32 v95, v80
	v_mov_b32_e32 v80, v89
	v_mov_b32_e32 v94, v88
	v_pk_mul_f32 v[80:81], v[80:81], v[90:91]
	v_mov_b32_e32 v91, v86
	v_mov_b32_e32 v86, v79
	v_pk_mul_f32 v[74:75], v[94:95], v[74:75]
	v_pk_mul_f32 v[88:89], v[80:81], v[80:81]
	v_mov_b32_e32 v90, v78
	v_pk_mul_f32 v[92:93], v[86:87], v[92:93]
	v_pk_fma_f32 v[88:89], v[74:75], v[74:75], v[88:89]
	v_pk_mul_f32 v[76:77], v[90:91], v[76:77]
	v_pk_mul_f32 v[78:79], v[92:93], v[92:93]
	v_add_f32_e32 v85, v88, v89
	v_pk_fma_f32 v[78:79], v[76:77], v[76:77], v[78:79]
	v_mov_b32_e32 v88, v74
	v_add_f32_e32 v79, v79, v85
	v_add_f32_e32 v78, v78, v79
	v_cndmask_b32_e64 v90, 0, v78, s[10:11]
	v_mov_b32_e32 v89, v80
	v_mov_b32_e32 v80, v75
	v_mov_b32_e32 v86, v77
	v_mov_b32_e32 v87, v93
	v_mov_b32_e32 v78, v76
	v_mov_b32_e32 v79, v92

; __device__ __forceinline__ float sigm(float x) { return __builtin_amdgcn_rcpf(1.f + __builtin_amdgcn_exp2f(-1.4426950408889634f * x)); }
; __device__ __forceinline__ float gelu_t(float x) { const float u = 0.7978845608028654f * (x + 0.044715f * x * x * x); return x * sigm(2.f * u); }
; __device__ __forceinline__ u32x4 pack8(f32x4 v0, f32x4 v1) { u32x4 w; w.x = cvt_pk_bf16(v0[0], v0[1]); w.y = cvt_pk_bf16(v0[2], v0[3]); w.z = cvt_pk_bf16(v1[0], v1[1]); w.w = cvt_pk_bf16(v1[2], v1[3]); return w; }
; template <class T> __device__ __forceinline__ void est(T* p, T v) { if constexpr (MK_EPI_NT != 0) __builtin_nontemporal_store(v, p); else *p = v; }
; __device__ __forceinline__ unsigned pk4_u8(f32x4 v) { return q8(v[0]) | (q8(v[1]) << 8) | (q8(v[2]) << 16) | (q8(v[3]) << 24); }
; __device__ __forceinline__ float sum8sq(f32x4 a, f32x4 b) { return (a[0] * a[0] + a[1] * a[1]) + (a[2] * a[2] + a[3] * a[3]) + (b[0] * b[0] + b[1] * b[1]) + (b[2] * b[2] + b[3] * b[3]); }
; __device__ __forceinline__ float ss_val(const ss_t* ss, int row) { return (float)ss[row] * (1.f / 16777216.f); }
;     __device__ __forceinline__ void operator()(AccT acc, const Unit& u, int wr, int wc, int fr, int fq) const {
;     ...
;             for (int m = 0; m < 4; ++m) { const int row = row0 + ai * 128 + m * 16; const float r = rsqrtf(ss_val(ss, row) * (1.0f / DM) + EPS); bf16_t* rp = O + (size_t)row * NIN + col0; float sq = 0.f;
; #pragma unroll
;                 for (int bj = 0; bj < 2; ++bj) { f32x4 v0 = acc[ai][bj][m][0] * r, v1 = acc[ai][bj][m][1] * r;
;                     if (type == 1 || type == 2) {
; #pragma unroll
;                         for (int j = 0; j < 4; ++j) { v0[j] = gelu_t(v0[j]); v1[j] = gelu_t(v1[j]); }
;                         if (type == 2) sq += sum8sq(v0, v1); }
;                     if (type == 3) {
; #pragma unroll
;                         for (int j = 0; j < 4; ++j) { v0[j] = sigm(v0[j]); v1[j] = sigm(v1[j]); }
;                         est((u32x2*)(G8 + (size_t)row * (NIN - C_G) + (col0 - C_G) + bj * 128), (u32x2)(u32x2){pk4_u8(v0), pk4_u8(v1)}); }
;                     else est((u32x4*)(rp + bj * 128), (u32x4)pack8(v0, v1)); }
;                 if (type == 2) row_atomic(ssv, row, sq, fq); }
.LBB0_1433:
	s_waitcnt lgkmcnt(0)
	s_nop 0
	s_and_b64 vcc, exec, s[12:13]
	s_waitcnt vmcnt(3)
	v_mov_b32_e32 v66, v248
	v_mov_b32_e32 v67, v249
	v_ffbh_u32_e32 v68, v67
	v_min_u32_e32 v68, 32, v68
	v_lshlrev_b64 v[66:67], v68, v[66:67]
	v_min_u32_e32 v66, 1, v66
	v_or_b32_e32 v66, v67, v66
	v_cvt_f32_u32_e32 v66, v66
	v_sub_u32_e32 v67, 32, v68
	v_ldexp_f32 v66, v66, v67
	v_mul_f32_e32 v66, 0x33800000, v66
	v_fmamk_f32 v66, v66, 0x3a000000, v164
	v_mul_f32_e32 v67, 0x4b800000, v66
	v_cmp_gt_f32_e64 s[16:17], s95, v66
	s_nop 1
	v_cndmask_b32_e64 v66, v66, v67, s[16:17]
	v_rsq_f32_e32 v66, v66
	s_nop 0
	v_mul_f32_e32 v67, 0x45800000, v66
	v_cndmask_b32_e64 v66, v66, v67, s[16:17]
	v_pk_mul_f32 v[64:65], v[64:65], v[66:67] op_sel_hi:[1,0]
	v_pk_mul_f32 v[72:73], v[62:63], v[66:67] op_sel_hi:[1,0]
	v_pk_mul_f32 v[68:69], v[60:61], v[66:67] op_sel_hi:[1,0]
	v_pk_mul_f32 v[70:71], v[58:59], v[66:67] op_sel_hi:[1,0]
	v_mov_b32_e32 v59, 0
	s_cbranch_vccnz .LBB0_1435
	v_mul_f32_e32 v59, 0x3d372713, v70
	v_mul_f32_e32 v59, v70, v59
	v_mul_f32_e32 v60, 0x3d372713, v73
	v_fma_f32 v59, v70, v59, v70
	v_mul_f32_e32 v60, v73, v60
	v_mul_f32_e32 v61, 0x3d372713, v71
	v_mul_f32_e32 v59, 0x3f4c422a, v59
	v_fma_f32 v60, v73, v60, v73
	v_mul_f32_e32 v61, v71, v61
	v_add_f32_e32 v59, v59, v59
	v_mul_f32_e32 v60, 0x3f4c422a, v60
	v_fma_f32 v61, v71, v61, v71
	v_mul_f32_e32 v59, 0xbfb8aa3b, v59
	v_add_f32_e32 v60, v60, v60
	v_mul_f32_e32 v61, 0x3f4c422a, v61
	v_exp_f32_e32 v59, v59
	v_mul_f32_e32 v60, 0xbfb8aa3b, v60
	v_add_f32_e32 v61, v61, v61
	v_exp_f32_e32 v60, v60
	v_mul_f32_e32 v61, 0xbfb8aa3b, v61
	v_exp_f32_e32 v63, v61
	v_add_f32_e32 v59, 1.0, v59
	v_rcp_f32_e32 v61, v59
	v_add_f32_e32 v59, 1.0, v60
	v_rcp_f32_e32 v62, v59
	v_add_f32_e32 v59, 1.0, v63
	v_mul_f32_e32 v60, 0x3d372713, v64
	v_mul_f32_e32 v63, 0x3d372713, v68
	v_mul_f32_e32 v60, v64, v60
	v_mul_f32_e32 v63, v68, v63
	v_fma_f32 v60, v64, v60, v64
	v_fma_f32 v63, v68, v63, v68
	v_mul_f32_e32 v60, 0x3f4c422a, v60
	v_mul_f32_e32 v63, 0x3f4c422a, v63
	v_add_f32_e32 v60, v60, v60
	v_add_f32_e32 v63, v63, v63
	v_mul_f32_e32 v60, 0xbfb8aa3b, v60
	v_mul_f32_e32 v63, 0xbfb8aa3b, v63
	v_exp_f32_e32 v60, v60
	v_exp_f32_e32 v63, v63
	v_rcp_f32_e32 v75, v59
	v_mul_f32_e32 v58, 0x3d372713, v72
	v_add_f32_e32 v59, 1.0, v60
	v_add_f32_e32 v60, 1.0, v63
	v_mul_f32_e32 v63, 0x3d372713, v65
	v_mul_f32_e32 v63, v65, v63
	v_mul_f32_e32 v67, 0x3d372713, v69
	v_mul_f32_e32 v58, v72, v58
	v_fma_f32 v63, v65, v63, v65
	v_mul_f32_e32 v67, v69, v67
	v_fma_f32 v58, v72, v58, v72
	v_mul_f32_e32 v63, 0x3f4c422a, v63
	v_fma_f32 v67, v69, v67, v69
	v_mul_f32_e32 v58, 0x3f4c422a, v58
	v_add_f32_e32 v63, v63, v63
	v_mul_f32_e32 v67, 0x3f4c422a, v67
	v_add_f32_e32 v58, v58, v58
	v_mul_f32_e32 v63, 0xbfb8aa3b, v63
	v_add_f32_e32 v67, v67, v67
	v_mul_f32_e32 v58, 0xbfb8aa3b, v58
	v_exp_f32_e32 v63, v63
	v_mul_f32_e32 v67, 0xbfb8aa3b, v67
	v_exp_f32_e32 v58, v58
	v_exp_f32_e32 v67, v67
	v_add_f32_e32 v63, 1.0, v63
	v_rcp_f32_e32 v63, v63
	v_add_f32_e32 v58, 1.0, v58
	v_add_f32_e32 v67, 1.0, v67
	v_rcp_f32_e32 v58, v58
	v_rcp_f32_e32 v59, v59
	v_rcp_f32_e32 v60, v60
	v_rcp_f32_e32 v74, v67
	v_mov_b32_e32 v77, v64
	v_mov_b32_e32 v64, v73
	v_mov_b32_e32 v76, v72
	v_pk_mul_f32 v[64:65], v[64:65], v[62:63]
	v_mov_b32_e32 v62, v68
	v_mov_b32_e32 v63, v70
	v_mov_b32_e32 v70, v69
	v_pk_mul_f32 v[76:77], v[76:77], v[58:59]
	v_pk_mul_f32 v[58:59], v[64:65], v[64:65]
	v_pk_mul_f32 v[60:61], v[62:63], v[60:61]
	v_pk_mul_f32 v[62:63], v[70:71], v[74:75]
	v_pk_fma_f32 v[58:59], v[76:77], v[76:77], v[58:59]
	v_pk_mul_f32 v[68:69], v[62:63], v[62:63]
	v_add_f32_e32 v58, v58, v59
	v_pk_fma_f32 v[68:69], v[60:61], v[60:61], v[68:69]
	v_mov_b32_e32 v72, v76
	v_add_f32_e32 v58, v69, v58
	v_add_f32_e32 v58, v68, v58
	v_cndmask_b32_e64 v59, 0, v58, s[10:11]
	v_mov_b32_e32 v73, v64
	v_mov_b32_e32 v64, v77
	v_mov_b32_e32 v70, v61
	v_mov_b32_e32 v71, v63
	v_mov_b32_e32 v68, v60
	v_mov_b32_e32 v69, v62

; __device__ __forceinline__ float sigm(float x) { return __builtin_amdgcn_rcpf(1.f + __builtin_amdgcn_exp2f(-1.4426950408889634f * x)); }
; __device__ __forceinline__ float gelu_t(float x) { const float u = 0.7978845608028654f * (x + 0.044715f * x * x * x); return x * sigm(2.f * u); }
; __device__ __forceinline__ u32x4 pack8(f32x4 v0, f32x4 v1) { u32x4 w; w.x = cvt_pk_bf16(v0[0], v0[1]); w.y = cvt_pk_bf16(v0[2], v0[3]); w.z = cvt_pk_bf16(v1[0], v1[1]); w.w = cvt_pk_bf16(v1[2], v1[3]); return w; }
; template <class T> __device__ __forceinline__ void est(T* p, T v) { if constexpr (MK_EPI_NT != 0) __builtin_nontemporal_store(v, p); else *p = v; }
; __device__ __forceinline__ unsigned pk4_u8(f32x4 v) { return q8(v[0]) | (q8(v[1]) << 8) | (q8(v[2]) << 16) | (q8(v[3]) << 24); }
; __device__ __forceinline__ float sum8sq(f32x4 a, f32x4 b) { return (a[0] * a[0] + a[1] * a[1]) + (a[2] * a[2] + a[3] * a[3]) + (b[0] * b[0] + b[1] * b[1]) + (b[2] * b[2] + b[3] * b[3]); }
; __device__ __forceinline__ float ss_val(const ss_t* ss, int row) { return (float)ss[row] * (1.f / 16777216.f); }
;     __device__ __forceinline__ void operator()(AccT acc, const Unit& u, int wr, int wc, int fr, int fq) const {
;     ...
;             for (int m = 0; m < 4; ++m) { const int row = row0 + ai * 128 + m * 16; const float r = rsqrtf(ss_val(ss, row) * (1.0f / DM) + EPS); bf16_t* rp = O + (size_t)row * NIN + col0; float sq = 0.f;
; #pragma unroll
;                 for (int bj = 0; bj < 2; ++bj) { f32x4 v0 = acc[ai][bj][m][0] * r, v1 = acc[ai][bj][m][1] * r;
;                     if (type == 1 || type == 2) {
; #pragma unroll
;                         for (int j = 0; j < 4; ++j) { v0[j] = gelu_t(v0[j]); v1[j] = gelu_t(v1[j]); }
;                         if (type == 2) sq += sum8sq(v0, v1); }
;                     if (type == 3) {
; #pragma unroll
;                         for (int j = 0; j < 4; ++j) { v0[j] = sigm(v0[j]); v1[j] = sigm(v1[j]); }
;                         est((u32x2*)(G8 + (size_t)row * (NIN - C_G) + (col0 - C_G) + bj * 128), (u32x2)(u32x2){pk4_u8(v0), pk4_u8(v1)}); }
;                     else est((u32x4*)(rp + bj * 128), (u32x4)pack8(v0, v1)); }
;                 if (type == 2) row_atomic(ssv, row, sq, fq); }
.LBB0_1451:
	s_waitcnt lgkmcnt(0)
	s_nop 0
	s_and_b64 vcc, exec, s[12:13]
	s_waitcnt vmcnt(2)
	v_mov_b32_e32 v50, v250
	v_mov_b32_e32 v51, v251
	v_ffbh_u32_e32 v52, v51
	v_min_u32_e32 v52, 32, v52
	v_lshlrev_b64 v[50:51], v52, v[50:51]
	v_min_u32_e32 v50, 1, v50
	v_or_b32_e32 v50, v51, v50
	v_cvt_f32_u32_e32 v50, v50
	v_sub_u32_e32 v51, 32, v52
	v_ldexp_f32 v50, v50, v51
	v_mul_f32_e32 v50, 0x33800000, v50
	v_fmamk_f32 v50, v50, 0x3a000000, v164
	v_mul_f32_e32 v51, 0x4b800000, v50
	v_cmp_gt_f32_e64 s[16:17], s95, v50
	s_nop 1
	v_cndmask_b32_e64 v50, v50, v51, s[16:17]
	v_rsq_f32_e32 v50, v50
	s_nop 0
	v_mul_f32_e32 v51, 0x45800000, v50
	v_cndmask_b32_e64 v50, v50, v51, s[16:17]
	v_pk_mul_f32 v[48:49], v[48:49], v[50:51] op_sel_hi:[1,0]
	v_pk_mul_f32 v[56:57], v[46:47], v[50:51] op_sel_hi:[1,0]
	v_pk_mul_f32 v[52:53], v[44:45], v[50:51] op_sel_hi:[1,0]
	v_pk_mul_f32 v[54:55], v[42:43], v[50:51] op_sel_hi:[1,0]
	v_mov_b32_e32 v43, 0
	s_cbranch_vccnz .LBB0_1453
	v_mul_f32_e32 v43, 0x3d372713, v54
	v_mul_f32_e32 v43, v54, v43
	v_mul_f32_e32 v44, 0x3d372713, v57
	v_fma_f32 v43, v54, v43, v54
	v_mul_f32_e32 v44, v57, v44
	v_mul_f32_e32 v45, 0x3d372713, v55
	v_mul_f32_e32 v43, 0x3f4c422a, v43
	v_fma_f32 v44, v57, v44, v57
	v_mul_f32_e32 v45, v55, v45
	v_add_f32_e32 v43, v43, v43
	v_mul_f32_e32 v44, 0x3f4c422a, v44
	v_fma_f32 v45, v55, v45, v55
	v_mul_f32_e32 v43, 0xbfb8aa3b, v43
	v_add_f32_e32 v44, v44, v44
	v_mul_f32_e32 v45, 0x3f4c422a, v45
	v_exp_f32_e32 v43, v43
	v_mul_f32_e32 v44, 0xbfb8aa3b, v44
	v_add_f32_e32 v45, v45, v45
	v_exp_f32_e32 v44, v44
	v_mul_f32_e32 v45, 0xbfb8aa3b, v45
	v_exp_f32_e32 v47, v45
	v_add_f32_e32 v43, 1.0, v43
	v_rcp_f32_e32 v45, v43
	v_add_f32_e32 v43, 1.0, v44
	v_rcp_f32_e32 v46, v43
	v_add_f32_e32 v43, 1.0, v47
	v_mul_f32_e32 v44, 0x3d372713, v48
	v_mul_f32_e32 v47, 0x3d372713, v52
	v_mul_f32_e32 v44, v48, v44
	v_mul_f32_e32 v47, v52, v47
	v_fma_f32 v44, v48, v44, v48
	v_fma_f32 v47, v52, v47, v52
	v_mul_f32_e32 v44, 0x3f4c422a, v44
	v_mul_f32_e32 v47, 0x3f4c422a, v47
	v_add_f32_e32 v44, v44, v44
	v_add_f32_e32 v47, v47, v47
	v_mul_f32_e32 v44, 0xbfb8aa3b, v44
	v_mul_f32_e32 v47, 0xbfb8aa3b, v47
	v_exp_f32_e32 v44, v44
	v_exp_f32_e32 v47, v47
	v_rcp_f32_e32 v59, v43
	v_mul_f32_e32 v42, 0x3d372713, v56
	v_add_f32_e32 v43, 1.0, v44
	v_add_f32_e32 v44, 1.0, v47
	v_mul_f32_e32 v47, 0x3d372713, v49
	v_mul_f32_e32 v47, v49, v47
	v_mul_f32_e32 v51, 0x3d372713, v53
	v_mul_f32_e32 v42, v56, v42
	v_fma_f32 v47, v49, v47, v49
	v_mul_f32_e32 v51, v53, v51
	v_fma_f32 v42, v56, v42, v56
	v_mul_f32_e32 v47, 0x3f4c422a, v47
	v_fma_f32 v51, v53, v51, v53
	v_mul_f32_e32 v42, 0x3f4c422a, v42
	v_add_f32_e32 v47, v47, v47
	v_mul_f32_e32 v51, 0x3f4c422a, v51
	v_add_f32_e32 v42, v42, v42
	v_mul_f32_e32 v47, 0xbfb8aa3b, v47
	v_add_f32_e32 v51, v51, v51
	v_mul_f32_e32 v42, 0xbfb8aa3b, v42
	v_exp_f32_e32 v47, v47
	v_mul_f32_e32 v51, 0xbfb8aa3b, v51
	v_exp_f32_e32 v42, v42
	v_exp_f32_e32 v51, v51
	v_add_f32_e32 v47, 1.0, v47
	v_rcp_f32_e32 v47, v47
	v_add_f32_e32 v42, 1.0, v42
	v_add_f32_e32 v51, 1.0, v51
	v_rcp_f32_e32 v42, v42
	v_rcp_f32_e32 v43, v43
	v_rcp_f32_e32 v44, v44
	v_rcp_f32_e32 v58, v51
	v_mov_b32_e32 v61, v48
	v_mov_b32_e32 v48, v57
	v_mov_b32_e32 v60, v56
	v_pk_mul_f32 v[48:49], v[48:49], v[46:47]
	v_mov_b32_e32 v46, v52
	v_mov_b32_e32 v47, v54
	v_mov_b32_e32 v54, v53
	v_pk_mul_f32 v[60:61], v[60:61], v[42:43]
	v_pk_mul_f32 v[42:43], v[48:49], v[48:49]
	v_pk_mul_f32 v[44:45], v[46:47], v[44:45]
	v_pk_mul_f32 v[46:47], v[54:55], v[58:59]
	v_pk_fma_f32 v[42:43], v[60:61], v[60:61], v[42:43]
	v_pk_mul_f32 v[52:53], v[46:47], v[46:47]
	v_add_f32_e32 v42, v42, v43
	v_pk_fma_f32 v[52:53], v[44:45], v[44:45], v[52:53]
	v_mov_b32_e32 v56, v60
	v_add_f32_e32 v42, v53, v42
	v_add_f32_e32 v42, v52, v42
	v_cndmask_b32_e64 v43, 0, v42, s[10:11]
	v_mov_b32_e32 v57, v48
	v_mov_b32_e32 v48, v61
	v_mov_b32_e32 v54, v45
	v_mov_b32_e32 v55, v47
	v_mov_b32_e32 v52, v44
	v_mov_b32_e32 v53, v46

; __device__ __forceinline__ float sigm(float x) { return __builtin_amdgcn_rcpf(1.f + __builtin_amdgcn_exp2f(-1.4426950408889634f * x)); }
; __device__ __forceinline__ float gelu_t(float x) { const float u = 0.7978845608028654f * (x + 0.044715f * x * x * x); return x * sigm(2.f * u); }
; __device__ __forceinline__ u32x4 pack8(f32x4 v0, f32x4 v1) { u32x4 w; w.x = cvt_pk_bf16(v0[0], v0[1]); w.y = cvt_pk_bf16(v0[2], v0[3]); w.z = cvt_pk_bf16(v1[0], v1[1]); w.w = cvt_pk_bf16(v1[2], v1[3]); return w; }
; template <class T> __device__ __forceinline__ void est(T* p, T v) { if constexpr (MK_EPI_NT != 0) __builtin_nontemporal_store(v, p); else *p = v; }
; __device__ __forceinline__ unsigned pk4_u8(f32x4 v) { return q8(v[0]) | (q8(v[1]) << 8) | (q8(v[2]) << 16) | (q8(v[3]) << 24); }
; __device__ __forceinline__ float sum8sq(f32x4 a, f32x4 b) { return (a[0] * a[0] + a[1] * a[1]) + (a[2] * a[2] + a[3] * a[3]) + (b[0] * b[0] + b[1] * b[1]) + (b[2] * b[2] + b[3] * b[3]); }
; __device__ __forceinline__ float ss_val(const ss_t* ss, int row) { return (float)ss[row] * (1.f / 16777216.f); }
;     __device__ __forceinline__ void operator()(AccT acc, const Unit& u, int wr, int wc, int fr, int fq) const {
;     ...
;             for (int m = 0; m < 4; ++m) { const int row = row0 + ai * 128 + m * 16; const float r = rsqrtf(ss_val(ss, row) * (1.0f / DM) + EPS); bf16_t* rp = O + (size_t)row * NIN + col0; float sq = 0.f;
; #pragma unroll
;                 for (int bj = 0; bj < 2; ++bj) { f32x4 v0 = acc[ai][bj][m][0] * r, v1 = acc[ai][bj][m][1] * r;
;                     if (type == 1 || type == 2) {
; #pragma unroll
;                         for (int j = 0; j < 4; ++j) { v0[j] = gelu_t(v0[j]); v1[j] = gelu_t(v1[j]); }
;                         if (type == 2) sq += sum8sq(v0, v1); }
;                     if (type == 3) {
; #pragma unroll
;                         for (int j = 0; j < 4; ++j) { v0[j] = sigm(v0[j]); v1[j] = sigm(v1[j]); }
;                         est((u32x2*)(G8 + (size_t)row * (NIN - C_G) + (col0 - C_G) + bj * 128), (u32x2)(u32x2){pk4_u8(v0), pk4_u8(v1)}); }
;                     else est((u32x4*)(rp + bj * 128), (u32x4)pack8(v0, v1)); }
;                 if (type == 2) row_atomic(ssv, row, sq, fq); }
.LBB0_1469:
	s_waitcnt lgkmcnt(0)
	s_nop 0
	s_and_b64 vcc, exec, s[12:13]
	s_waitcnt vmcnt(1)
	v_mov_b32_e32 v34, v252
	v_mov_b32_e32 v35, v253
	v_ffbh_u32_e32 v36, v35
	v_min_u32_e32 v36, 32, v36
	v_lshlrev_b64 v[34:35], v36, v[34:35]
	v_min_u32_e32 v34, 1, v34
	v_or_b32_e32 v34, v35, v34
	v_cvt_f32_u32_e32 v34, v34
	v_sub_u32_e32 v35, 32, v36
	v_ldexp_f32 v34, v34, v35
	v_mul_f32_e32 v34, 0x33800000, v34
	v_fmamk_f32 v34, v34, 0x3a000000, v164
	v_mul_f32_e32 v35, 0x4b800000, v34
	v_cmp_gt_f32_e64 s[16:17], s95, v34
	s_nop 1
	v_cndmask_b32_e64 v34, v34, v35, s[16:17]
	v_rsq_f32_e32 v34, v34
	s_nop 0
	v_mul_f32_e32 v35, 0x45800000, v34
	v_cndmask_b32_e64 v34, v34, v35, s[16:17]
	v_pk_mul_f32 v[32:33], v[32:33], v[34:35] op_sel_hi:[1,0]
	v_pk_mul_f32 v[40:41], v[30:31], v[34:35] op_sel_hi:[1,0]
	v_pk_mul_f32 v[36:37], v[28:29], v[34:35] op_sel_hi:[1,0]
	v_pk_mul_f32 v[38:39], v[26:27], v[34:35] op_sel_hi:[1,0]
	v_mov_b32_e32 v27, 0
	s_cbranch_vccnz .LBB0_1471
	v_mul_f32_e32 v27, 0x3d372713, v38
	v_mul_f32_e32 v27, v38, v27
	v_mul_f32_e32 v28, 0x3d372713, v41
	v_fma_f32 v27, v38, v27, v38
	v_mul_f32_e32 v28, v41, v28
	v_mul_f32_e32 v29, 0x3d372713, v39
	v_mul_f32_e32 v27, 0x3f4c422a, v27
	v_fma_f32 v28, v41, v28, v41
	v_mul_f32_e32 v29, v39, v29
	v_add_f32_e32 v27, v27, v27
	v_mul_f32_e32 v28, 0x3f4c422a, v28
	v_fma_f32 v29, v39, v29, v39
	v_mul_f32_e32 v27, 0xbfb8aa3b, v27
	v_add_f32_e32 v28, v28, v28
	v_mul_f32_e32 v29, 0x3f4c422a, v29
	v_exp_f32_e32 v27, v27
	v_mul_f32_e32 v28, 0xbfb8aa3b, v28
	v_add_f32_e32 v29, v29, v29
	v_exp_f32_e32 v28, v28
	v_mul_f32_e32 v29, 0xbfb8aa3b, v29
	v_exp_f32_e32 v31, v29
	v_add_f32_e32 v27, 1.0, v27
	v_rcp_f32_e32 v29, v27
	v_add_f32_e32 v27, 1.0, v28
	v_rcp_f32_e32 v30, v27
	v_add_f32_e32 v27, 1.0, v31
	v_mul_f32_e32 v28, 0x3d372713, v32
	v_mul_f32_e32 v31, 0x3d372713, v36
	v_mul_f32_e32 v28, v32, v28
	v_mul_f32_e32 v31, v36, v31
	v_fma_f32 v28, v32, v28, v32
	v_fma_f32 v31, v36, v31, v36
	v_mul_f32_e32 v28, 0x3f4c422a, v28
	v_mul_f32_e32 v31, 0x3f4c422a, v31
	v_add_f32_e32 v28, v28, v28
	v_add_f32_e32 v31, v31, v31
	v_mul_f32_e32 v28, 0xbfb8aa3b, v28
	v_mul_f32_e32 v31, 0xbfb8aa3b, v31
	v_exp_f32_e32 v28, v28
	v_exp_f32_e32 v31, v31
	v_rcp_f32_e32 v43, v27
	v_mul_f32_e32 v26, 0x3d372713, v40
	v_add_f32_e32 v27, 1.0, v28
	v_add_f32_e32 v28, 1.0, v31
	v_mul_f32_e32 v31, 0x3d372713, v33
	v_mul_f32_e32 v31, v33, v31
	v_mul_f32_e32 v35, 0x3d372713, v37
	v_mul_f32_e32 v26, v40, v26
	v_fma_f32 v31, v33, v31, v33
	v_mul_f32_e32 v35, v37, v35
	v_fma_f32 v26, v40, v26, v40
	v_mul_f32_e32 v31, 0x3f4c422a, v31
	v_fma_f32 v35, v37, v35, v37
	v_mul_f32_e32 v26, 0x3f4c422a, v26
	v_add_f32_e32 v31, v31, v31
	v_mul_f32_e32 v35, 0x3f4c422a, v35
	v_add_f32_e32 v26, v26, v26
	v_mul_f32_e32 v31, 0xbfb8aa3b, v31
	v_add_f32_e32 v35, v35, v35
	v_mul_f32_e32 v26, 0xbfb8aa3b, v26
	v_exp_f32_e32 v31, v31
	v_mul_f32_e32 v35, 0xbfb8aa3b, v35
	v_exp_f32_e32 v26, v26
	v_exp_f32_e32 v35, v35
	v_add_f32_e32 v31, 1.0, v31
	v_rcp_f32_e32 v31, v31
	v_add_f32_e32 v26, 1.0, v26
	v_add_f32_e32 v35, 1.0, v35
	v_rcp_f32_e32 v26, v26
	v_rcp_f32_e32 v27, v27
	v_rcp_f32_e32 v28, v28
	v_rcp_f32_e32 v42, v35
	v_mov_b32_e32 v45, v32
	v_mov_b32_e32 v32, v41
	v_mov_b32_e32 v44, v40
	v_pk_mul_f32 v[32:33], v[32:33], v[30:31]
	v_mov_b32_e32 v30, v36
	v_mov_b32_e32 v31, v38
	v_mov_b32_e32 v38, v37
	v_pk_mul_f32 v[44:45], v[44:45], v[26:27]
	v_pk_mul_f32 v[26:27], v[32:33], v[32:33]
	v_pk_mul_f32 v[28:29], v[30:31], v[28:29]
	v_pk_mul_f32 v[30:31], v[38:39], v[42:43]
	v_pk_fma_f32 v[26:27], v[44:45], v[44:45], v[26:27]
	v_pk_mul_f32 v[36:37], v[30:31], v[30:31]
	v_add_f32_e32 v26, v26, v27
	v_pk_fma_f32 v[36:37], v[28:29], v[28:29], v[36:37]
	v_mov_b32_e32 v40, v44
	v_add_f32_e32 v26, v37, v26
	v_add_f32_e32 v26, v36, v26
	v_cndmask_b32_e64 v27, 0, v26, s[10:11]
	v_mov_b32_e32 v41, v32
	v_mov_b32_e32 v32, v45
	v_mov_b32_e32 v38, v29
	v_mov_b32_e32 v39, v31
	v_mov_b32_e32 v36, v28
	v_mov_b32_e32 v37, v30

; __device__ __forceinline__ float sigm(float x) { return __builtin_amdgcn_rcpf(1.f + __builtin_amdgcn_exp2f(-1.4426950408889634f * x)); }
; __device__ __forceinline__ float gelu_t(float x) { const float u = 0.7978845608028654f * (x + 0.044715f * x * x * x); return x * sigm(2.f * u); }
; __device__ __forceinline__ u32x4 pack8(f32x4 v0, f32x4 v1) { u32x4 w; w.x = cvt_pk_bf16(v0[0], v0[1]); w.y = cvt_pk_bf16(v0[2], v0[3]); w.z = cvt_pk_bf16(v1[0], v1[1]); w.w = cvt_pk_bf16(v1[2], v1[3]); return w; }
; template <class T> __device__ __forceinline__ void est(T* p, T v) { if constexpr (MK_EPI_NT != 0) __builtin_nontemporal_store(v, p); else *p = v; }
; __device__ __forceinline__ unsigned pk4_u8(f32x4 v) { return q8(v[0]) | (q8(v[1]) << 8) | (q8(v[2]) << 16) | (q8(v[3]) << 24); }
; __device__ __forceinline__ float sum8sq(f32x4 a, f32x4 b) { return (a[0] * a[0] + a[1] * a[1]) + (a[2] * a[2] + a[3] * a[3]) + (b[0] * b[0] + b[1] * b[1]) + (b[2] * b[2] + b[3] * b[3]); }
; __device__ __forceinline__ float ss_val(const ss_t* ss, int row) { return (float)ss[row] * (1.f / 16777216.f); }
;     __device__ __forceinline__ void operator()(AccT acc, const Unit& u, int wr, int wc, int fr, int fq) const {
;     ...
;             for (int m = 0; m < 4; ++m) { const int row = row0 + ai * 128 + m * 16; const float r = rsqrtf(ss_val(ss, row) * (1.0f / DM) + EPS); bf16_t* rp = O + (size_t)row * NIN + col0; float sq = 0.f;
; #pragma unroll
;                 for (int bj = 0; bj < 2; ++bj) { f32x4 v0 = acc[ai][bj][m][0] * r, v1 = acc[ai][bj][m][1] * r;
;                     if (type == 1 || type == 2) {
; #pragma unroll
;                         for (int j = 0; j < 4; ++j) { v0[j] = gelu_t(v0[j]); v1[j] = gelu_t(v1[j]); }
;                         if (type == 2) sq += sum8sq(v0, v1); }
;                     if (type == 3) {
; #pragma unroll
;                         for (int j = 0; j < 4; ++j) { v0[j] = sigm(v0[j]); v1[j] = sigm(v1[j]); }
;                         est((u32x2*)(G8 + (size_t)row * (NIN - C_G) + (col0 - C_G) + bj * 128), (u32x2)(u32x2){pk4_u8(v0), pk4_u8(v1)}); }
;                     else est((u32x4*)(rp + bj * 128), (u32x4)pack8(v0, v1)); }
;                 if (type == 2) row_atomic(ssv, row, sq, fq); }
.LBB0_1487:
	s_waitcnt lgkmcnt(0)
	s_nop 0
	s_and_b64 vcc, exec, s[12:13]
	s_waitcnt vmcnt(0)
	v_mov_b32_e32 v18, v254
	v_mov_b32_e32 v19, v255
	v_ffbh_u32_e32 v20, v19
	v_min_u32_e32 v20, 32, v20
	v_lshlrev_b64 v[18:19], v20, v[18:19]
	v_min_u32_e32 v18, 1, v18
	v_or_b32_e32 v18, v19, v18
	v_cvt_f32_u32_e32 v18, v18
	v_sub_u32_e32 v19, 32, v20
	v_ldexp_f32 v18, v18, v19
	v_mul_f32_e32 v18, 0x33800000, v18
	v_fmamk_f32 v18, v18, 0x3a000000, v164
	v_mul_f32_e32 v19, 0x4b800000, v18
	v_cmp_gt_f32_e64 s[16:17], s95, v18
	s_nop 1
	v_cndmask_b32_e64 v18, v18, v19, s[16:17]
	v_rsq_f32_e32 v18, v18
	s_nop 0
	v_mul_f32_e32 v19, 0x45800000, v18
	v_cndmask_b32_e64 v18, v18, v19, s[16:17]
	v_pk_mul_f32 v[16:17], v[16:17], v[18:19] op_sel_hi:[1,0]
	v_pk_mul_f32 v[24:25], v[14:15], v[18:19] op_sel_hi:[1,0]
	v_pk_mul_f32 v[20:21], v[12:13], v[18:19] op_sel_hi:[1,0]
	v_pk_mul_f32 v[22:23], v[10:11], v[18:19] op_sel_hi:[1,0]
	v_mov_b32_e32 v11, 0
	s_cbranch_vccnz .LBB0_1489
	v_mul_f32_e32 v11, 0x3d372713, v22
	v_mul_f32_e32 v11, v22, v11
	v_mul_f32_e32 v12, 0x3d372713, v25
	v_fma_f32 v11, v22, v11, v22
	v_mul_f32_e32 v12, v25, v12
	v_mul_f32_e32 v13, 0x3d372713, v23
	v_mul_f32_e32 v11, 0x3f4c422a, v11
	v_fma_f32 v12, v25, v12, v25
	v_mul_f32_e32 v13, v23, v13
	v_add_f32_e32 v11, v11, v11
	v_mul_f32_e32 v12, 0x3f4c422a, v12
	v_fma_f32 v13, v23, v13, v23
	v_mul_f32_e32 v11, 0xbfb8aa3b, v11
	v_add_f32_e32 v12, v12, v12
	v_mul_f32_e32 v13, 0x3f4c422a, v13
	v_exp_f32_e32 v11, v11
	v_mul_f32_e32 v12, 0xbfb8aa3b, v12
	v_add_f32_e32 v13, v13, v13
	v_exp_f32_e32 v12, v12
	v_mul_f32_e32 v13, 0xbfb8aa3b, v13
	v_exp_f32_e32 v15, v13
	v_add_f32_e32 v11, 1.0, v11
	v_rcp_f32_e32 v13, v11
	v_add_f32_e32 v11, 1.0, v12
	v_rcp_f32_e32 v14, v11
	v_add_f32_e32 v11, 1.0, v15
	v_mul_f32_e32 v12, 0x3d372713, v16
	v_mul_f32_e32 v15, 0x3d372713, v20
	v_mul_f32_e32 v12, v16, v12
	v_mul_f32_e32 v15, v20, v15
	v_fma_f32 v12, v16, v12, v16
	v_fma_f32 v15, v20, v15, v20
	v_mul_f32_e32 v12, 0x3f4c422a, v12
	v_mul_f32_e32 v15, 0x3f4c422a, v15
	v_add_f32_e32 v12, v12, v12
	v_add_f32_e32 v15, v15, v15
	v_mul_f32_e32 v12, 0xbfb8aa3b, v12
	v_mul_f32_e32 v15, 0xbfb8aa3b, v15
	v_exp_f32_e32 v12, v12
	v_exp_f32_e32 v15, v15
	v_rcp_f32_e32 v27, v11
	v_mul_f32_e32 v10, 0x3d372713, v24
	v_add_f32_e32 v11, 1.0, v12
	v_add_f32_e32 v12, 1.0, v15
	v_mul_f32_e32 v15, 0x3d372713, v17
	v_mul_f32_e32 v15, v17, v15
	v_mul_f32_e32 v19, 0x3d372713, v21
	v_mul_f32_e32 v10, v24, v10
	v_fma_f32 v15, v17, v15, v17
	v_mul_f32_e32 v19, v21, v19
	v_fma_f32 v10, v24, v10, v24
	v_mul_f32_e32 v15, 0x3f4c422a, v15
	v_fma_f32 v19, v21, v19, v21
	v_mul_f32_e32 v10, 0x3f4c422a, v10
	v_add_f32_e32 v15, v15, v15
	v_mul_f32_e32 v19, 0x3f4c422a, v19
	v_add_f32_e32 v10, v10, v10
	v_mul_f32_e32 v15, 0xbfb8aa3b, v15
	v_add_f32_e32 v19, v19, v19
	v_mul_f32_e32 v10, 0xbfb8aa3b, v10
	v_exp_f32_e32 v15, v15
	v_mul_f32_e32 v19, 0xbfb8aa3b, v19
	v_exp_f32_e32 v10, v10
	v_exp_f32_e32 v19, v19
	v_add_f32_e32 v15, 1.0, v15
	v_rcp_f32_e32 v15, v15
	v_add_f32_e32 v10, 1.0, v10
	v_add_f32_e32 v19, 1.0, v19
	v_rcp_f32_e32 v10, v10
	v_rcp_f32_e32 v11, v11
	v_rcp_f32_e32 v12, v12
	v_rcp_f32_e32 v26, v19
	v_mov_b32_e32 v29, v16
	v_mov_b32_e32 v16, v25
	v_mov_b32_e32 v28, v24
	v_pk_mul_f32 v[16:17], v[16:17], v[14:15]
	v_mov_b32_e32 v14, v20
	v_mov_b32_e32 v15, v22
	v_mov_b32_e32 v22, v21
	v_pk_mul_f32 v[28:29], v[28:29], v[10:11]
	v_pk_mul_f32 v[10:11], v[16:17], v[16:17]
	v_pk_mul_f32 v[12:13], v[14:15], v[12:13]
	v_pk_mul_f32 v[14:15], v[22:23], v[26:27]
	v_pk_fma_f32 v[10:11], v[28:29], v[28:29], v[10:11]
	v_pk_mul_f32 v[20:21], v[14:15], v[14:15]
	v_add_f32_e32 v10, v10, v11
	v_pk_fma_f32 v[20:21], v[12:13], v[12:13], v[20:21]
	v_mov_b32_e32 v24, v28
	v_add_f32_e32 v10, v21, v10
	v_add_f32_e32 v10, v20, v10
	v_cndmask_b32_e64 v11, 0, v10, s[10:11]
	v_mov_b32_e32 v25, v16
	v_mov_b32_e32 v16, v29
	v_mov_b32_e32 v22, v13
	v_mov_b32_e32 v23, v15
	v_mov_b32_e32 v20, v12
	v_mov_b32_e32 v21, v14
